# speedup vs baseline: 1.0238x; 1.0238x over previous
.Lmy_noperm_in:
	v_mfma_f32_16x16x32_f16 v[210:213], v[70:73], v[150:153], v[98:101]
	v_mfma_f32_16x16x32_f16 v[214:217], v[74:77], v[150:153], v[102:105]
	v_mfma_f32_16x16x32_f16 v[210:213], v[66:69], v[154:157], v[210:213]
	v_mfma_f32_16x16x32_f16 v[214:217], v[78:81], v[154:157], v[214:217]
	s_add_u32 s48, s20, 0x600000
	s_addc_u32 s49, s21, 0
	s_sub_u32 s50, s22, 0x600000
	s_mov_b32 s51, s23
	s_add_u32 s68, s16, 0xc000
	s_addc_u32 s69, s17, 0
	s_sub_u32 s70, s18, 0xc000
	s_mov_b32 s71, s19
	s_add_u32 s52, s20, 0x700000
	s_addc_u32 s53, s21, 0
	s_sub_u32 s54, s22, 0x700000
	s_mov_b32 s55, s23
	s_add_u32 s72, s16, 0x10000
	s_addc_u32 s73, s17, 0
	s_sub_u32 s74, s18, 0x10000
	s_mov_b32 s75, s19
	s_add_u32 s56, s20, 0x800000
	s_addc_u32 s57, s21, 0
	s_sub_u32 s58, s22, 0x800000
	s_mov_b32 s59, s23
	s_add_u32 s76, s16, 0x14000
	s_addc_u32 s77, s17, 0
	s_sub_u32 s78, s18, 0x14000
	s_mov_b32 s79, s19
	s_add_u32 s60, s20, 0x900000
	s_addc_u32 s61, s21, 0
	s_sub_u32 s62, s22, 0x900000
	s_mov_b32 s63, s23
	s_add_u32 s80, s16, 0x18000
	s_addc_u32 s81, s17, 0
	s_sub_u32 s82, s18, 0x18000
	s_mov_b32 s83, s19
	ds_read_b128 v[158:161], v248 offset:0
	ds_read_b128 v[162:165], v248 offset:1024
	ds_read_b128 v[166:169], v249 offset:2048
	ds_read_b128 v[170:173], v249 offset:3072
	v_mfma_f32_16x16x32_f16 v[218:221], v[82:85], v[150:153], v[106:109]
	v_mfma_f32_16x16x32_f16 v[222:225], v[90:93], v[150:153], v[110:113]
	v_mfma_f32_16x16x32_f16 v[218:221], v[86:89], v[154:157], v[218:221]
	v_mfma_f32_16x16x32_f16 v[222:225], v[94:97], v[154:157], v[222:225]
	s_waitcnt lgkmcnt(2)
	v_mfma_f32_16x16x32_f16 v[210:213], v[54:57], v[158:161], v[210:213]
	v_mfma_f32_16x16x32_f16 v[210:213], v[58:61], v[162:165], v[210:213]
	s_waitcnt lgkmcnt(0)
	v_mfma_f32_16x16x32_f16 v[210:213], v[62:65], v[166:169], v[210:213]
	v_mfma_f32_16x16x32_f16 v[210:213], v[50:53], v[170:173], v[210:213]
	s_waitcnt vmcnt(9)
	v_cvt_pk_f16_f32 v251, v196, v197
	ds_write_b32 v1, v251 offset:4096
	ds_read_b128 v[150:153], v186 offset:2048
	ds_read_b128 v[154:157], v186 offset:3072
	s_add_i32 s45, s45, 0x100000
	s_add_i32 s46, s46, 0x4000
	s_movk_i32 s47, 0x0
	s_add_i32 s43, s40, -12
	s_lshl_b32 s43, s43, 12
	s_cmp_lt_u32 s40, 14
	s_cselect_b32 s43, s47, s43
	v_exp_f32_e32 v226, v210
	v_exp_f32_e32 v227, v211
	v_mfma_f32_16x16x32_f16 v[214:217], v[34:37], v[158:161], v[214:217]
	v_min_f32_e32 v228, s42, v212
	v_exp_f32_e32 v229, v213
	v_mfma_f32_16x16x32_f16 v[214:217], v[38:41], v[162:165], v[214:217]
	v_exp_f32_e32 v228, v228
	v_add_f32_e32 v227, 1.0, v227
	v_mfma_f32_16x16x32_f16 v[214:217], v[42:45], v[166:169], v[214:217]
	v_fma_f32 v230, v228, s41, s41
	v_rcp_f32_e32 v227, v227
	v_mfma_f32_16x16x32_f16 v[214:217], v[46:49], v[170:173], v[214:217]
	v_fma_f32 v230, v226, v230, v230
	v_rcp_f32_e32 v230, v230
	v_mfma_f32_16x16x32_f16 v[218:221], v[18:21], v[158:161], v[218:221]
	v_fma_f32 v226, -v228, v230, v230
	v_fma_f32 v200, v200, v227, v226
	v_mfma_f32_16x16x32_f16 v[218:221], v[14:17], v[162:165], v[218:221]
	v_min_f32_e32 v226, s42, v200
	v_exp_f32_e32 v226, v226
	v_mfma_f32_16x16x32_f16 v[218:221], v[10:13], v[166:169], v[218:221]
	v_add_f32_e32 v227, 1.0, v226
	v_fma_f32 v227, v229, v227, v227
	v_mfma_f32_16x16x32_f16 v[218:221], v[26:29], v[170:173], v[218:221]
	v_rcp_f32_e32 v227, v227
	v_exp_f32_e32 v231, v214
	v_mfma_f32_16x16x32_f16 v[222:225], v[2:5], v[158:161], v[222:225]
	v_exp_f32_e32 v232, v215
	v_fma_f32 v226, -v226, v227, v227
	v_mfma_f32_16x16x32_f16 v[222:225], v[6:9], v[162:165], v[222:225]
	v_min_f32_e32 v233, s42, v216
	v_exp_f32_e32 v234, v217
	v_mfma_f32_16x16x32_f16 v[222:225], v[22:25], v[166:169], v[222:225]
	v_exp_f32_e32 v236, v218
	v_exp_f32_e32 v233, v233
	v_mfma_f32_16x16x32_f16 v[222:225], v[30:33], v[170:173], v[222:225]
	v_add_f32_e32 v232, 1.0, v232
	v_exp_f32_e32 v227, v219
	v_fma_f32 v235, v233, s41, s41
	v_rcp_f32_e32 v232, v232
	v_min_f32_e32 v228, s42, v220
	v_fma_f32 v235, v231, v235, v235
	v_rcp_f32_e32 v235, v235
	v_exp_f32_e32 v229, v221
	v_fma_f32 v231, -v233, v235, v235
	v_fma_f32 v201, v201, v232, v231
	v_exp_f32_e32 v228, v228
	v_min_f32_e32 v231, s42, v201
	v_exp_f32_e32 v231, v231
	v_add_f32_e32 v227, 1.0, v227
	v_add_f32_e32 v232, 1.0, v231
	v_mfma_f32_16x16x32_f16 v[146:149], v[138:141], v[158:161], v[146:149]
	v_fma_f32 v232, v234, v232, v232
	v_fma_f32 v230, v228, s41, s41
	v_rcp_f32_e32 v232, v232
	v_mfma_f32_16x16x32_f16 v[146:149], v[142:145], v[162:165], v[146:149]
	v_fma_f32 v231, -v231, v232, v232
	v_rcp_f32_e32 v227, v227
	v_cvt_pk_f16_f32 v246, v226, v231
	buffer_load_dwordx4 v[138:141], v189, s[16:19], s46 offen
	buffer_load_dwordx4 v[142:145], v208, s[16:19], s46 offen
	v_exp_f32_e32 v231, v222
	v_fma_f32 v230, v236, v230, v230
	v_exp_f32_e32 v232, v223
	s_waitcnt lgkmcnt(0)
	v_mfma_f32_16x16x32_f16 v[210:213], v[70:73], v[150:153], v[98:101]
	v_min_f32_e32 v233, s42, v224
	v_rcp_f32_e32 v230, v230
	v_exp_f32_e32 v234, v225
	v_mfma_f32_16x16x32_f16 v[214:217], v[74:77], v[150:153], v[102:105]
	v_exp_f32_e32 v233, v233
	v_fma_f32 v236, -v228, v230, v230
	v_add_f32_e32 v232, 1.0, v232
	v_fma_f32 v235, v233, s41, s41
	v_fma_f32 v198, v198, v227, v236
	v_rcp_f32_e32 v232, v232
	v_fma_f32 v235, v231, v235, v235
	v_min_f32_e32 v236, s42, v198
	v_rcp_f32_e32 v235, v235
	s_nop 0
	v_fma_f32 v231, -v233, v235, v235
	v_exp_f32_e32 v236, v236
	v_fma_f32 v199, v199, v232, v231
	v_min_f32_e32 v231, s42, v199
	v_add_f32_e32 v227, 1.0, v236
	v_exp_f32_e32 v231, v231
	v_fma_f32 v227, v229, v227, v227
	v_add_u32_e32 v250, s43, v206
	v_add_f32_e32 v232, 1.0, v231
	v_rcp_f32_e32 v227, v227
	v_add_u32_e32 v248, s43, v252
	v_fma_f32 v232, v234, v232, v232
	v_fma_f32 v236, -v236, v227, v227
	v_add_u32_e32 v249, s43, v253
	v_rcp_f32_e32 v232, v232
	s_nop 0
	v_fma_f32 v231, -v231, v232, v232
	v_cvt_pk_f16_f32 v247, v236, v231
	ds_write_b64 v250, v[246:247] offset:8192
	v_mfma_f32_16x16x32_f16 v[210:213], v[66:69], v[154:157], v[210:213]
	v_mfma_f32_16x16x32_f16 v[214:217], v[78:81], v[154:157], v[214:217]
	v_mov_b32_e32 v174, v246
	v_mov_b32_e32 v175, v247
	buffer_load_dwordx2 v[196:197], v209, s[20:23], s45 offen
	s_add_i32 s40, s40, 1
	s_add_i32 s44, s44, 0x1000
	s_waitcnt lgkmcnt(0)
	s_barrier
	ds_read_b128 v[158:161], v248 offset:0
	ds_read_b128 v[162:165], v248 offset:1024
	ds_read_b128 v[166:169], v249 offset:2048
	ds_read_b128 v[170:173], v249 offset:3072
	v_mfma_f32_16x16x32_f16 v[218:221], v[82:85], v[150:153], v[106:109]
	v_mfma_f32_16x16x32_f16 v[222:225], v[90:93], v[150:153], v[110:113]
	v_mfma_f32_16x16x32_f16 v[218:221], v[86:89], v[154:157], v[218:221]
	v_mfma_f32_16x16x32_f16 v[222:225], v[94:97], v[154:157], v[222:225]
	s_waitcnt lgkmcnt(2)
	v_mfma_f32_16x16x32_f16 v[210:213], v[54:57], v[158:161], v[210:213]
	v_mfma_f32_16x16x32_f16 v[210:213], v[58:61], v[162:165], v[210:213]
	s_waitcnt lgkmcnt(0)
	v_mfma_f32_16x16x32_f16 v[210:213], v[62:65], v[166:169], v[210:213]
	v_mfma_f32_16x16x32_f16 v[210:213], v[50:53], v[170:173], v[210:213]
	s_waitcnt vmcnt(9)
	v_cvt_pk_f16_f32 v251, v194, v195
	ds_write_b32 v1, v251 offset:6144
	ds_read_b128 v[150:153], v186 offset:4096
	ds_read_b128 v[154:157], v186 offset:5120
	s_add_i32 s45, s45, 0x100000
	s_add_i32 s46, s46, 0x4000
	s_movk_i32 s47, 0x1000
	s_add_i32 s43, s40, -12
	s_lshl_b32 s43, s43, 12
	s_cmp_lt_u32 s40, 14
	s_cselect_b32 s43, s47, s43
	v_exp_f32_e32 v226, v210
	v_exp_f32_e32 v227, v211
	v_mfma_f32_16x16x32_f16 v[214:217], v[34:37], v[158:161], v[214:217]
	v_min_f32_e32 v228, s42, v212
	v_exp_f32_e32 v229, v213
	v_mfma_f32_16x16x32_f16 v[214:217], v[38:41], v[162:165], v[214:217]
	v_exp_f32_e32 v228, v228
	v_add_f32_e32 v227, 1.0, v227
	v_mfma_f32_16x16x32_f16 v[214:217], v[42:45], v[166:169], v[214:217]
	v_fma_f32 v230, v228, s41, s41
	v_rcp_f32_e32 v227, v227
	v_mfma_f32_16x16x32_f16 v[214:217], v[46:49], v[170:173], v[214:217]
	v_fma_f32 v230, v226, v230, v230
	v_rcp_f32_e32 v230, v230
	v_mfma_f32_16x16x32_f16 v[218:221], v[18:21], v[158:161], v[218:221]
	v_fma_f32 v226, -v228, v230, v230
	v_fma_f32 v200, v200, v227, v226
	v_mfma_f32_16x16x32_f16 v[218:221], v[14:17], v[162:165], v[218:221]
	v_min_f32_e32 v226, s42, v200
	v_exp_f32_e32 v226, v226
	v_mfma_f32_16x16x32_f16 v[218:221], v[10:13], v[166:169], v[218:221]
	v_add_f32_e32 v227, 1.0, v226
	v_fma_f32 v227, v229, v227, v227
	v_mfma_f32_16x16x32_f16 v[218:221], v[26:29], v[170:173], v[218:221]
	v_rcp_f32_e32 v227, v227
	v_exp_f32_e32 v231, v214
	v_mfma_f32_16x16x32_f16 v[222:225], v[2:5], v[158:161], v[222:225]
	v_exp_f32_e32 v232, v215
	v_fma_f32 v226, -v226, v227, v227
	v_mfma_f32_16x16x32_f16 v[222:225], v[6:9], v[162:165], v[222:225]
	v_min_f32_e32 v233, s42, v216
	v_exp_f32_e32 v234, v217
	v_mfma_f32_16x16x32_f16 v[222:225], v[22:25], v[166:169], v[222:225]
	v_exp_f32_e32 v236, v218
	v_exp_f32_e32 v233, v233
	v_mfma_f32_16x16x32_f16 v[222:225], v[30:33], v[170:173], v[222:225]
	v_add_f32_e32 v232, 1.0, v232
	v_exp_f32_e32 v227, v219
	v_fma_f32 v235, v233, s41, s41
	v_rcp_f32_e32 v232, v232
	v_min_f32_e32 v228, s42, v220
	v_fma_f32 v235, v231, v235, v235
	v_rcp_f32_e32 v235, v235
	v_exp_f32_e32 v229, v221
	v_fma_f32 v231, -v233, v235, v235
	v_fma_f32 v201, v201, v232, v231
	v_exp_f32_e32 v228, v228
	v_min_f32_e32 v231, s42, v201
	v_exp_f32_e32 v231, v231
	v_add_f32_e32 v227, 1.0, v227
	v_add_f32_e32 v232, 1.0, v231
	v_mfma_f32_16x16x32_f16 v[146:149], v[130:133], v[158:161], v[146:149]
	v_fma_f32 v232, v234, v232, v232
	v_fma_f32 v230, v228, s41, s41
	v_rcp_f32_e32 v232, v232
	v_mfma_f32_16x16x32_f16 v[146:149], v[134:137], v[162:165], v[146:149]
	v_fma_f32 v231, -v231, v232, v232
	v_rcp_f32_e32 v227, v227
	v_cvt_pk_f16_f32 v246, v226, v231
	buffer_load_dwordx4 v[130:133], v189, s[16:19], s46 offen
	buffer_load_dwordx4 v[134:137], v208, s[16:19], s46 offen
	v_exp_f32_e32 v231, v222
	v_fma_f32 v230, v236, v230, v230
	v_exp_f32_e32 v232, v223
	s_waitcnt lgkmcnt(0)
	v_mfma_f32_16x16x32_f16 v[210:213], v[70:73], v[150:153], v[98:101]
	v_min_f32_e32 v233, s42, v224
	v_rcp_f32_e32 v230, v230
	v_exp_f32_e32 v234, v225
	v_mfma_f32_16x16x32_f16 v[214:217], v[74:77], v[150:153], v[102:105]
	v_exp_f32_e32 v233, v233
	v_fma_f32 v236, -v228, v230, v230
	v_add_f32_e32 v232, 1.0, v232
	v_fma_f32 v235, v233, s41, s41
	v_fma_f32 v198, v198, v227, v236
	v_rcp_f32_e32 v232, v232
	v_fma_f32 v235, v231, v235, v235
	v_min_f32_e32 v236, s42, v198
	v_rcp_f32_e32 v235, v235
	s_nop 0
	v_fma_f32 v231, -v233, v235, v235
	v_exp_f32_e32 v236, v236
	v_fma_f32 v199, v199, v232, v231
	v_min_f32_e32 v231, s42, v199
	v_add_f32_e32 v227, 1.0, v236
	v_exp_f32_e32 v231, v231
	v_fma_f32 v227, v229, v227, v227
	v_add_u32_e32 v250, s43, v206
	v_add_f32_e32 v232, 1.0, v231
	v_rcp_f32_e32 v227, v227
	v_add_u32_e32 v248, s43, v252
	v_fma_f32 v232, v234, v232, v232
	v_fma_f32 v236, -v236, v227, v227
	v_add_u32_e32 v249, s43, v253
	v_rcp_f32_e32 v232, v232
	s_nop 0
	v_fma_f32 v231, -v231, v232, v232
	v_cvt_pk_f16_f32 v247, v236, v231
	ds_write_b64 v250, v[246:247] offset:8192
	v_mfma_f32_16x16x32_f16 v[210:213], v[66:69], v[154:157], v[210:213]
	v_mfma_f32_16x16x32_f16 v[214:217], v[78:81], v[154:157], v[214:217]
	v_mov_b32_e32 v176, v246
	v_mov_b32_e32 v177, v247
	buffer_load_dwordx2 v[194:195], v209, s[20:23], s45 offen
	s_add_i32 s40, s40, 1
	s_add_i32 s44, s44, 0x1000
	s_waitcnt lgkmcnt(0)
	s_barrier
	ds_read_b128 v[158:161], v248 offset:0
	ds_read_b128 v[162:165], v248 offset:1024
	ds_read_b128 v[166:169], v249 offset:2048
	ds_read_b128 v[170:173], v249 offset:3072
	v_mfma_f32_16x16x32_f16 v[218:221], v[82:85], v[150:153], v[106:109]
	v_mfma_f32_16x16x32_f16 v[222:225], v[90:93], v[150:153], v[110:113]
	v_mfma_f32_16x16x32_f16 v[218:221], v[86:89], v[154:157], v[218:221]
	v_mfma_f32_16x16x32_f16 v[222:225], v[94:97], v[154:157], v[222:225]
	s_waitcnt lgkmcnt(2)
	v_mfma_f32_16x16x32_f16 v[210:213], v[54:57], v[158:161], v[210:213]
	v_mfma_f32_16x16x32_f16 v[210:213], v[58:61], v[162:165], v[210:213]
	s_waitcnt lgkmcnt(0)
	v_mfma_f32_16x16x32_f16 v[210:213], v[62:65], v[166:169], v[210:213]
	v_mfma_f32_16x16x32_f16 v[210:213], v[50:53], v[170:173], v[210:213]
	s_waitcnt vmcnt(9)
	v_cvt_pk_f16_f32 v251, v192, v193
	ds_write_b32 v1, v251 offset:0
	ds_read_b128 v[150:153], v186 offset:6144
	ds_read_b128 v[154:157], v186 offset:7168
	s_add_i32 s45, s45, 0x100000
	s_add_i32 s46, s46, 0x4000
	s_movk_i32 s47, 0x0
	s_add_i32 s43, s40, -12
	s_lshl_b32 s43, s43, 12
	s_cmp_lt_u32 s40, 14
	s_cselect_b32 s43, s47, s43
	v_exp_f32_e32 v226, v210
	v_exp_f32_e32 v227, v211
	v_mfma_f32_16x16x32_f16 v[214:217], v[34:37], v[158:161], v[214:217]
	v_min_f32_e32 v228, s42, v212
	v_exp_f32_e32 v229, v213
	v_mfma_f32_16x16x32_f16 v[214:217], v[38:41], v[162:165], v[214:217]
	v_exp_f32_e32 v228, v228
	v_add_f32_e32 v227, 1.0, v227
	v_mfma_f32_16x16x32_f16 v[214:217], v[42:45], v[166:169], v[214:217]
	v_fma_f32 v230, v228, s41, s41
	v_rcp_f32_e32 v227, v227
	v_mfma_f32_16x16x32_f16 v[214:217], v[46:49], v[170:173], v[214:217]
	v_fma_f32 v230, v226, v230, v230
	v_rcp_f32_e32 v230, v230
	v_mfma_f32_16x16x32_f16 v[218:221], v[18:21], v[158:161], v[218:221]
	v_fma_f32 v226, -v228, v230, v230
	v_fma_f32 v200, v200, v227, v226
	v_mfma_f32_16x16x32_f16 v[218:221], v[14:17], v[162:165], v[218:221]
	v_min_f32_e32 v226, s42, v200
	v_exp_f32_e32 v226, v226
	v_mfma_f32_16x16x32_f16 v[218:221], v[10:13], v[166:169], v[218:221]
	v_add_f32_e32 v227, 1.0, v226
	v_fma_f32 v227, v229, v227, v227
	v_mfma_f32_16x16x32_f16 v[218:221], v[26:29], v[170:173], v[218:221]
	v_rcp_f32_e32 v227, v227
	v_exp_f32_e32 v231, v214
	v_mfma_f32_16x16x32_f16 v[222:225], v[2:5], v[158:161], v[222:225]
	v_exp_f32_e32 v232, v215
	v_fma_f32 v226, -v226, v227, v227
	v_mfma_f32_16x16x32_f16 v[222:225], v[6:9], v[162:165], v[222:225]
	v_min_f32_e32 v233, s42, v216
	v_exp_f32_e32 v234, v217
	v_mfma_f32_16x16x32_f16 v[222:225], v[22:25], v[166:169], v[222:225]
	v_exp_f32_e32 v236, v218
	v_exp_f32_e32 v233, v233
	v_mfma_f32_16x16x32_f16 v[222:225], v[30:33], v[170:173], v[222:225]
	v_add_f32_e32 v232, 1.0, v232
	v_exp_f32_e32 v227, v219
	v_fma_f32 v235, v233, s41, s41
	v_rcp_f32_e32 v232, v232
	v_min_f32_e32 v228, s42, v220
	v_fma_f32 v235, v231, v235, v235
	v_rcp_f32_e32 v235, v235
	v_exp_f32_e32 v229, v221
	v_fma_f32 v231, -v233, v235, v235
	v_fma_f32 v201, v201, v232, v231
	v_exp_f32_e32 v228, v228
	v_min_f32_e32 v231, s42, v201
	v_exp_f32_e32 v231, v231
	v_add_f32_e32 v227, 1.0, v227
	v_add_f32_e32 v232, 1.0, v231
	v_mfma_f32_16x16x32_f16 v[146:149], v[122:125], v[158:161], v[146:149]
	v_fma_f32 v232, v234, v232, v232
	v_fma_f32 v230, v228, s41, s41
	v_rcp_f32_e32 v232, v232
	v_mfma_f32_16x16x32_f16 v[146:149], v[126:129], v[162:165], v[146:149]
	v_fma_f32 v231, -v231, v232, v232
	v_rcp_f32_e32 v227, v227
	v_cvt_pk_f16_f32 v246, v226, v231
	buffer_load_dwordx4 v[122:125], v189, s[16:19], s46 offen
	buffer_load_dwordx4 v[126:129], v208, s[16:19], s46 offen
	v_exp_f32_e32 v231, v222
	v_fma_f32 v230, v236, v230, v230
	v_exp_f32_e32 v232, v223
	s_waitcnt lgkmcnt(0)
	v_mfma_f32_16x16x32_f16 v[210:213], v[70:73], v[150:153], v[98:101]
	v_min_f32_e32 v233, s42, v224
	v_rcp_f32_e32 v230, v230
	v_exp_f32_e32 v234, v225
	v_mfma_f32_16x16x32_f16 v[214:217], v[74:77], v[150:153], v[102:105]
	v_exp_f32_e32 v233, v233
	v_fma_f32 v236, -v228, v230, v230
	v_add_f32_e32 v232, 1.0, v232
	v_fma_f32 v235, v233, s41, s41
	v_fma_f32 v198, v198, v227, v236
	v_rcp_f32_e32 v232, v232
	v_fma_f32 v235, v231, v235, v235
	v_min_f32_e32 v236, s42, v198
	v_rcp_f32_e32 v235, v235
	s_nop 0
	v_fma_f32 v231, -v233, v235, v235
	v_exp_f32_e32 v236, v236
	v_fma_f32 v199, v199, v232, v231
	v_min_f32_e32 v231, s42, v199
	v_add_f32_e32 v227, 1.0, v236
	v_exp_f32_e32 v231, v231
	v_fma_f32 v227, v229, v227, v227
	v_add_u32_e32 v250, s43, v206
	v_add_f32_e32 v232, 1.0, v231
	v_rcp_f32_e32 v227, v227
	v_add_u32_e32 v248, s43, v252
	v_fma_f32 v232, v234, v232, v232
	v_fma_f32 v236, -v236, v227, v227
	v_add_u32_e32 v249, s43, v253
	v_rcp_f32_e32 v232, v232
	s_nop 0
	v_fma_f32 v231, -v231, v232, v232
	v_cvt_pk_f16_f32 v247, v236, v231
	ds_write_b64 v250, v[246:247] offset:8192
	v_mfma_f32_16x16x32_f16 v[210:213], v[66:69], v[154:157], v[210:213]
	v_mfma_f32_16x16x32_f16 v[214:217], v[78:81], v[154:157], v[214:217]
	v_mov_b32_e32 v178, v246
	v_mov_b32_e32 v179, v247
	buffer_load_dwordx2 v[192:193], v209, s[20:23], s45 offen
	s_add_i32 s40, s40, 1
	s_add_i32 s44, s44, 0x1000
	s_waitcnt lgkmcnt(0)
	s_barrier
	ds_read_b128 v[158:161], v248 offset:0
	ds_read_b128 v[162:165], v248 offset:1024
	ds_read_b128 v[166:169], v249 offset:2048
	ds_read_b128 v[170:173], v249 offset:3072
	v_mfma_f32_16x16x32_f16 v[218:221], v[82:85], v[150:153], v[106:109]
	v_mfma_f32_16x16x32_f16 v[222:225], v[90:93], v[150:153], v[110:113]
	v_mfma_f32_16x16x32_f16 v[218:221], v[86:89], v[154:157], v[218:221]
	v_mfma_f32_16x16x32_f16 v[222:225], v[94:97], v[154:157], v[222:225]
	s_waitcnt lgkmcnt(2)
	v_mfma_f32_16x16x32_f16 v[210:213], v[54:57], v[158:161], v[210:213]
	v_mfma_f32_16x16x32_f16 v[210:213], v[58:61], v[162:165], v[210:213]
	s_waitcnt lgkmcnt(0)
	v_mfma_f32_16x16x32_f16 v[210:213], v[62:65], v[166:169], v[210:213]
	v_mfma_f32_16x16x32_f16 v[210:213], v[50:53], v[170:173], v[210:213]
	s_waitcnt vmcnt(9)
	v_cvt_pk_f16_f32 v251, v190, v191
	ds_write_b32 v1, v251 offset:2048
	ds_read_b128 v[150:153], v186 offset:0
	ds_read_b128 v[154:157], v186 offset:1024
	s_add_i32 s45, s45, 0x100000
	s_add_i32 s46, s46, 0x4000
	s_movk_i32 s47, 0x1000
	s_add_i32 s43, s40, -12
	s_lshl_b32 s43, s43, 12
	s_cmp_lt_u32 s40, 14
	s_cselect_b32 s43, s47, s43
	v_exp_f32_e32 v226, v210
	v_exp_f32_e32 v227, v211
	v_mfma_f32_16x16x32_f16 v[214:217], v[34:37], v[158:161], v[214:217]
	v_min_f32_e32 v228, s42, v212
	v_exp_f32_e32 v229, v213
	v_mfma_f32_16x16x32_f16 v[214:217], v[38:41], v[162:165], v[214:217]
	v_exp_f32_e32 v228, v228
	v_add_f32_e32 v227, 1.0, v227
	v_mfma_f32_16x16x32_f16 v[214:217], v[42:45], v[166:169], v[214:217]
	v_fma_f32 v230, v228, s41, s41
	v_rcp_f32_e32 v227, v227
	v_mfma_f32_16x16x32_f16 v[214:217], v[46:49], v[170:173], v[214:217]
	v_fma_f32 v230, v226, v230, v230
	v_rcp_f32_e32 v230, v230
	v_mfma_f32_16x16x32_f16 v[218:221], v[18:21], v[158:161], v[218:221]
	v_fma_f32 v226, -v228, v230, v230
	v_fma_f32 v200, v200, v227, v226
	v_mfma_f32_16x16x32_f16 v[218:221], v[14:17], v[162:165], v[218:221]
	v_min_f32_e32 v226, s42, v200
	v_exp_f32_e32 v226, v226
	v_mfma_f32_16x16x32_f16 v[218:221], v[10:13], v[166:169], v[218:221]
	v_add_f32_e32 v227, 1.0, v226
	v_fma_f32 v227, v229, v227, v227
	v_mfma_f32_16x16x32_f16 v[218:221], v[26:29], v[170:173], v[218:221]
	v_rcp_f32_e32 v227, v227
	v_exp_f32_e32 v231, v214
	v_mfma_f32_16x16x32_f16 v[222:225], v[2:5], v[158:161], v[222:225]
	v_exp_f32_e32 v232, v215
	v_fma_f32 v226, -v226, v227, v227
	v_mfma_f32_16x16x32_f16 v[222:225], v[6:9], v[162:165], v[222:225]
	v_min_f32_e32 v233, s42, v216
	v_exp_f32_e32 v234, v217
	v_mfma_f32_16x16x32_f16 v[222:225], v[22:25], v[166:169], v[222:225]
	v_exp_f32_e32 v236, v218
	v_exp_f32_e32 v233, v233
	v_mfma_f32_16x16x32_f16 v[222:225], v[30:33], v[170:173], v[222:225]
	v_add_f32_e32 v232, 1.0, v232
	v_exp_f32_e32 v227, v219
	v_fma_f32 v235, v233, s41, s41
	v_rcp_f32_e32 v232, v232
	v_min_f32_e32 v228, s42, v220
	v_fma_f32 v235, v231, v235, v235
	v_rcp_f32_e32 v235, v235
	v_exp_f32_e32 v229, v221
	v_fma_f32 v231, -v233, v235, v235
	v_fma_f32 v201, v201, v232, v231
	v_exp_f32_e32 v228, v228
	v_min_f32_e32 v231, s42, v201
	v_exp_f32_e32 v231, v231
	v_add_f32_e32 v227, 1.0, v227
	v_add_f32_e32 v232, 1.0, v231
	v_mfma_f32_16x16x32_f16 v[146:149], v[114:117], v[158:161], v[146:149]
	v_fma_f32 v232, v234, v232, v232
	v_fma_f32 v230, v228, s41, s41
	v_rcp_f32_e32 v232, v232
	v_mfma_f32_16x16x32_f16 v[146:149], v[118:121], v[162:165], v[146:149]
	v_fma_f32 v231, -v231, v232, v232
	v_rcp_f32_e32 v227, v227
	v_cvt_pk_f16_f32 v246, v226, v231
	buffer_load_dwordx4 v[114:117], v189, s[16:19], s46 offen
	buffer_load_dwordx4 v[118:121], v208, s[16:19], s46 offen
	v_exp_f32_e32 v231, v222
	v_fma_f32 v230, v236, v230, v230
	v_exp_f32_e32 v232, v223
	s_waitcnt lgkmcnt(0)
	v_mfma_f32_16x16x32_f16 v[210:213], v[70:73], v[150:153], v[98:101]
	v_min_f32_e32 v233, s42, v224
	v_rcp_f32_e32 v230, v230
	v_exp_f32_e32 v234, v225
	v_mfma_f32_16x16x32_f16 v[214:217], v[74:77], v[150:153], v[102:105]
	v_exp_f32_e32 v233, v233
	v_fma_f32 v236, -v228, v230, v230
	v_add_f32_e32 v232, 1.0, v232
	v_fma_f32 v235, v233, s41, s41
	v_fma_f32 v198, v198, v227, v236
	v_rcp_f32_e32 v232, v232
	v_fma_f32 v235, v231, v235, v235
	v_min_f32_e32 v236, s42, v198
	v_rcp_f32_e32 v235, v235
	s_nop 0
	v_fma_f32 v231, -v233, v235, v235
	v_exp_f32_e32 v236, v236
	v_fma_f32 v199, v199, v232, v231
	v_min_f32_e32 v231, s42, v199
	v_add_f32_e32 v227, 1.0, v236
	v_exp_f32_e32 v231, v231
	v_fma_f32 v227, v229, v227, v227
	v_add_u32_e32 v250, s43, v206
	v_add_f32_e32 v232, 1.0, v231
	v_rcp_f32_e32 v227, v227
	v_add_u32_e32 v248, s43, v252
	v_fma_f32 v232, v234, v232, v232
	v_fma_f32 v236, -v236, v227, v227
	v_add_u32_e32 v249, s43, v253
	v_rcp_f32_e32 v232, v232
	s_nop 0
	v_fma_f32 v231, -v231, v232, v232
	v_cvt_pk_f16_f32 v247, v236, v231
	ds_write_b64 v250, v[246:247] offset:8192
	v_mfma_f32_16x16x32_f16 v[210:213], v[66:69], v[154:157], v[210:213]
	v_mfma_f32_16x16x32_f16 v[214:217], v[78:81], v[154:157], v[214:217]
	v_mov_b32_e32 v180, v246
	v_mov_b32_e32 v181, v247
	buffer_load_dwordx2 v[190:191], v209, s[20:23], s45 offen
	s_add_i32 s40, s40, 1
	s_add_i32 s44, s44, 0x1000
	s_waitcnt lgkmcnt(0)
	s_barrier
	ds_read_b128 v[158:161], v248 offset:0
	ds_read_b128 v[162:165], v248 offset:1024
	ds_read_b128 v[166:169], v249 offset:2048
	ds_read_b128 v[170:173], v249 offset:3072
	v_mfma_f32_16x16x32_f16 v[218:221], v[82:85], v[150:153], v[106:109]
	v_mfma_f32_16x16x32_f16 v[222:225], v[90:93], v[150:153], v[110:113]
	v_mfma_f32_16x16x32_f16 v[218:221], v[86:89], v[154:157], v[218:221]
	v_mfma_f32_16x16x32_f16 v[222:225], v[94:97], v[154:157], v[222:225]
	s_waitcnt lgkmcnt(2)
	v_mfma_f32_16x16x32_f16 v[210:213], v[54:57], v[158:161], v[210:213]
	v_mfma_f32_16x16x32_f16 v[210:213], v[58:61], v[162:165], v[210:213]
	s_waitcnt lgkmcnt(0)
	v_mfma_f32_16x16x32_f16 v[210:213], v[62:65], v[166:169], v[210:213]
	v_mfma_f32_16x16x32_f16 v[210:213], v[50:53], v[170:173], v[210:213]
	s_waitcnt vmcnt(9)
	v_cvt_pk_f16_f32 v251, v196, v197
	ds_write_b32 v1, v251 offset:4096
	ds_read_b128 v[150:153], v186 offset:2048
	ds_read_b128 v[154:157], v186 offset:3072
	s_add_i32 s45, s45, 0x100000
	s_add_i32 s46, s46, 0x4000
	s_movk_i32 s47, 0x0
	s_add_i32 s43, s40, -12
	s_lshl_b32 s43, s43, 12
	s_cmp_lt_u32 s40, 14
	s_cselect_b32 s43, s47, s43
	v_exp_f32_e32 v226, v210
	v_exp_f32_e32 v227, v211
	v_mfma_f32_16x16x32_f16 v[214:217], v[34:37], v[158:161], v[214:217]
	v_min_f32_e32 v228, s42, v212
	v_exp_f32_e32 v229, v213
	v_mfma_f32_16x16x32_f16 v[214:217], v[38:41], v[162:165], v[214:217]
	v_exp_f32_e32 v228, v228
	v_add_f32_e32 v227, 1.0, v227
	v_mfma_f32_16x16x32_f16 v[214:217], v[42:45], v[166:169], v[214:217]
	v_fma_f32 v230, v228, s41, s41
	v_rcp_f32_e32 v227, v227
	v_mfma_f32_16x16x32_f16 v[214:217], v[46:49], v[170:173], v[214:217]
	v_fma_f32 v230, v226, v230, v230
	v_rcp_f32_e32 v230, v230
	v_mfma_f32_16x16x32_f16 v[218:221], v[18:21], v[158:161], v[218:221]
	v_fma_f32 v226, -v228, v230, v230
	v_fma_f32 v200, v200, v227, v226
	v_mfma_f32_16x16x32_f16 v[218:221], v[14:17], v[162:165], v[218:221]
	v_min_f32_e32 v226, s42, v200
	v_exp_f32_e32 v226, v226
	v_mfma_f32_16x16x32_f16 v[218:221], v[10:13], v[166:169], v[218:221]
	v_add_f32_e32 v227, 1.0, v226
	v_fma_f32 v227, v229, v227, v227
	v_mfma_f32_16x16x32_f16 v[218:221], v[26:29], v[170:173], v[218:221]
	v_rcp_f32_e32 v227, v227
	v_exp_f32_e32 v231, v214
	v_mfma_f32_16x16x32_f16 v[222:225], v[2:5], v[158:161], v[222:225]
	v_exp_f32_e32 v232, v215
	v_fma_f32 v226, -v226, v227, v227
	v_mfma_f32_16x16x32_f16 v[222:225], v[6:9], v[162:165], v[222:225]
	v_min_f32_e32 v233, s42, v216
	v_exp_f32_e32 v234, v217
	v_mfma_f32_16x16x32_f16 v[222:225], v[22:25], v[166:169], v[222:225]
	v_exp_f32_e32 v236, v218
	v_exp_f32_e32 v233, v233
	v_mfma_f32_16x16x32_f16 v[222:225], v[30:33], v[170:173], v[222:225]
	v_add_f32_e32 v232, 1.0, v232
	v_exp_f32_e32 v227, v219
	v_fma_f32 v235, v233, s41, s41
	v_rcp_f32_e32 v232, v232
	v_min_f32_e32 v228, s42, v220
	v_fma_f32 v235, v231, v235, v235
	v_rcp_f32_e32 v235, v235
	v_exp_f32_e32 v229, v221
	v_fma_f32 v231, -v233, v235, v235
	v_fma_f32 v201, v201, v232, v231
	v_exp_f32_e32 v228, v228
	v_min_f32_e32 v231, s42, v201
	v_exp_f32_e32 v231, v231
	v_add_f32_e32 v227, 1.0, v227
	v_add_f32_e32 v232, 1.0, v231
	v_mfma_f32_16x16x32_f16 v[146:149], v[138:141], v[158:161], v[146:149]
	v_fma_f32 v232, v234, v232, v232
	v_fma_f32 v230, v228, s41, s41
	v_rcp_f32_e32 v232, v232
	v_mfma_f32_16x16x32_f16 v[146:149], v[142:145], v[162:165], v[146:149]
	v_fma_f32 v231, -v231, v232, v232
	v_rcp_f32_e32 v227, v227
	v_cvt_pk_f16_f32 v246, v226, v231
	buffer_load_dwordx4 v[138:141], v189, s[16:19], s46 offen
	buffer_load_dwordx4 v[142:145], v208, s[16:19], s46 offen
	v_exp_f32_e32 v231, v222
	v_fma_f32 v230, v236, v230, v230
	v_exp_f32_e32 v232, v223
	s_waitcnt lgkmcnt(0)
	v_mfma_f32_16x16x32_f16 v[210:213], v[70:73], v[150:153], v[98:101]
	v_min_f32_e32 v233, s42, v224
	v_rcp_f32_e32 v230, v230
	v_exp_f32_e32 v234, v225
	v_mfma_f32_16x16x32_f16 v[214:217], v[74:77], v[150:153], v[102:105]
	v_exp_f32_e32 v233, v233
	v_fma_f32 v236, -v228, v230, v230
	v_add_f32_e32 v232, 1.0, v232
	v_fma_f32 v235, v233, s41, s41
	v_fma_f32 v198, v198, v227, v236
	v_rcp_f32_e32 v232, v232
	v_fma_f32 v235, v231, v235, v235
	v_min_f32_e32 v236, s42, v198
	v_rcp_f32_e32 v235, v235
	s_nop 0
	v_fma_f32 v231, -v233, v235, v235
	v_exp_f32_e32 v236, v236
	v_fma_f32 v199, v199, v232, v231
	v_min_f32_e32 v231, s42, v199
	v_add_f32_e32 v227, 1.0, v236
	v_exp_f32_e32 v231, v231
	v_fma_f32 v227, v229, v227, v227
	v_add_u32_e32 v250, s43, v206
	v_add_f32_e32 v232, 1.0, v231
	v_rcp_f32_e32 v227, v227
	v_add_u32_e32 v248, s43, v252
	v_fma_f32 v232, v234, v232, v232
	v_fma_f32 v236, -v236, v227, v227
	v_add_u32_e32 v249, s43, v253
	v_rcp_f32_e32 v232, v232
	s_nop 0
	v_fma_f32 v231, -v231, v232, v232
	v_cvt_pk_f16_f32 v247, v236, v231
	ds_write_b64 v250, v[246:247] offset:8192
	v_mfma_f32_16x16x32_f16 v[210:213], v[66:69], v[154:157], v[210:213]
	v_mfma_f32_16x16x32_f16 v[214:217], v[78:81], v[154:157], v[214:217]
	v_mov_b32_e32 v182, v246
	v_mov_b32_e32 v183, v247
	buffer_load_dwordx2 v[196:197], v209, s[20:23], s45 offen
	s_add_i32 s40, s40, 1
	s_add_i32 s44, s44, 0x1000
	s_waitcnt lgkmcnt(0)
	s_barrier
	ds_read_b128 v[158:161], v248 offset:0
	ds_read_b128 v[162:165], v248 offset:1024
	ds_read_b128 v[166:169], v249 offset:2048
	ds_read_b128 v[170:173], v249 offset:3072
	v_mfma_f32_16x16x32_f16 v[218:221], v[82:85], v[150:153], v[106:109]
	v_mfma_f32_16x16x32_f16 v[222:225], v[90:93], v[150:153], v[110:113]
	v_mfma_f32_16x16x32_f16 v[218:221], v[86:89], v[154:157], v[218:221]
	v_mfma_f32_16x16x32_f16 v[222:225], v[94:97], v[154:157], v[222:225]
	s_waitcnt lgkmcnt(2)
	v_mfma_f32_16x16x32_f16 v[210:213], v[54:57], v[158:161], v[210:213]
	v_mfma_f32_16x16x32_f16 v[210:213], v[58:61], v[162:165], v[210:213]
	s_waitcnt lgkmcnt(0)
	v_mfma_f32_16x16x32_f16 v[210:213], v[62:65], v[166:169], v[210:213]
	v_mfma_f32_16x16x32_f16 v[210:213], v[50:53], v[170:173], v[210:213]
	s_waitcnt vmcnt(9)
	v_cvt_pk_f16_f32 v251, v194, v195
	ds_write_b32 v1, v251 offset:6144
	ds_read_b128 v[150:153], v186 offset:4096
	ds_read_b128 v[154:157], v186 offset:5120
	s_add_i32 s45, s45, 0x100000
	s_add_i32 s46, s46, 0x4000
	s_movk_i32 s47, 0x1000
	s_add_i32 s43, s40, -12
	s_lshl_b32 s43, s43, 12
	s_cmp_lt_u32 s40, 14
	s_cselect_b32 s43, s47, s43
	v_exp_f32_e32 v226, v210
	v_exp_f32_e32 v227, v211
	v_mfma_f32_16x16x32_f16 v[214:217], v[34:37], v[158:161], v[214:217]
	v_min_f32_e32 v228, s42, v212
	v_exp_f32_e32 v229, v213
	v_mfma_f32_16x16x32_f16 v[214:217], v[38:41], v[162:165], v[214:217]
	v_exp_f32_e32 v228, v228
	v_add_f32_e32 v227, 1.0, v227
	v_mfma_f32_16x16x32_f16 v[214:217], v[42:45], v[166:169], v[214:217]
	v_fma_f32 v230, v228, s41, s41
	v_rcp_f32_e32 v227, v227
	v_mfma_f32_16x16x32_f16 v[214:217], v[46:49], v[170:173], v[214:217]
	v_fma_f32 v230, v226, v230, v230
	v_rcp_f32_e32 v230, v230
	v_mfma_f32_16x16x32_f16 v[218:221], v[18:21], v[158:161], v[218:221]
	v_fma_f32 v226, -v228, v230, v230
	v_fma_f32 v200, v200, v227, v226
	v_mfma_f32_16x16x32_f16 v[218:221], v[14:17], v[162:165], v[218:221]
	v_min_f32_e32 v226, s42, v200
	v_exp_f32_e32 v226, v226
	v_mfma_f32_16x16x32_f16 v[218:221], v[10:13], v[166:169], v[218:221]
	v_add_f32_e32 v227, 1.0, v226
	v_fma_f32 v227, v229, v227, v227
	v_mfma_f32_16x16x32_f16 v[218:221], v[26:29], v[170:173], v[218:221]
	v_rcp_f32_e32 v227, v227
	v_exp_f32_e32 v231, v214
	v_mfma_f32_16x16x32_f16 v[222:225], v[2:5], v[158:161], v[222:225]
	v_exp_f32_e32 v232, v215
	v_fma_f32 v226, -v226, v227, v227
	v_mfma_f32_16x16x32_f16 v[222:225], v[6:9], v[162:165], v[222:225]
	v_min_f32_e32 v233, s42, v216
	v_exp_f32_e32 v234, v217
	v_mfma_f32_16x16x32_f16 v[222:225], v[22:25], v[166:169], v[222:225]
	v_exp_f32_e32 v236, v218
	v_exp_f32_e32 v233, v233
	v_mfma_f32_16x16x32_f16 v[222:225], v[30:33], v[170:173], v[222:225]
	v_add_f32_e32 v232, 1.0, v232
	v_exp_f32_e32 v227, v219
	v_fma_f32 v235, v233, s41, s41
	v_rcp_f32_e32 v232, v232
	v_min_f32_e32 v228, s42, v220
	v_fma_f32 v235, v231, v235, v235
	v_rcp_f32_e32 v235, v235
	v_exp_f32_e32 v229, v221
	v_fma_f32 v231, -v233, v235, v235
	v_fma_f32 v201, v201, v232, v231
	v_exp_f32_e32 v228, v228
	v_min_f32_e32 v231, s42, v201
	v_exp_f32_e32 v231, v231
	v_add_f32_e32 v227, 1.0, v227
	v_add_f32_e32 v232, 1.0, v231
	v_mfma_f32_16x16x32_f16 v[146:149], v[130:133], v[158:161], v[146:149]
	v_fma_f32 v232, v234, v232, v232
	v_fma_f32 v230, v228, s41, s41
	v_rcp_f32_e32 v232, v232
	v_mfma_f32_16x16x32_f16 v[146:149], v[134:137], v[162:165], v[146:149]
	v_fma_f32 v231, -v231, v232, v232
	v_rcp_f32_e32 v227, v227
	v_cvt_pk_f16_f32 v246, v226, v231
	buffer_load_dwordx4 v[130:133], v189, s[16:19], s46 offen
	buffer_load_dwordx4 v[134:137], v208, s[16:19], s46 offen
	v_exp_f32_e32 v231, v222
	v_fma_f32 v230, v236, v230, v230
	v_exp_f32_e32 v232, v223
	s_waitcnt lgkmcnt(0)
	v_mfma_f32_16x16x32_f16 v[210:213], v[70:73], v[150:153], v[98:101]
	v_min_f32_e32 v233, s42, v224
	v_rcp_f32_e32 v230, v230
	v_exp_f32_e32 v234, v225
	v_mfma_f32_16x16x32_f16 v[214:217], v[74:77], v[150:153], v[102:105]
	v_exp_f32_e32 v233, v233
	v_fma_f32 v236, -v228, v230, v230
	v_add_f32_e32 v232, 1.0, v232
	v_fma_f32 v235, v233, s41, s41
	v_fma_f32 v198, v198, v227, v236
	v_rcp_f32_e32 v232, v232
	v_fma_f32 v235, v231, v235, v235
	v_min_f32_e32 v236, s42, v198
	v_rcp_f32_e32 v235, v235
	s_nop 0
	v_fma_f32 v231, -v233, v235, v235
	v_exp_f32_e32 v236, v236
	v_fma_f32 v199, v199, v232, v231
	v_min_f32_e32 v231, s42, v199
	v_add_f32_e32 v227, 1.0, v236
	v_exp_f32_e32 v231, v231
	v_fma_f32 v227, v229, v227, v227
	v_add_u32_e32 v250, s43, v206
	v_add_f32_e32 v232, 1.0, v231
	v_rcp_f32_e32 v227, v227
	v_add_u32_e32 v248, s43, v252
	v_fma_f32 v232, v234, v232, v232
	v_fma_f32 v236, -v236, v227, v227
	v_add_u32_e32 v249, s43, v253
	v_rcp_f32_e32 v232, v232
	s_nop 0
	v_fma_f32 v231, -v231, v232, v232
	v_cvt_pk_f16_f32 v247, v236, v231
	ds_write_b64 v250, v[246:247] offset:8192
	v_mfma_f32_16x16x32_f16 v[210:213], v[66:69], v[154:157], v[210:213]
	v_mfma_f32_16x16x32_f16 v[214:217], v[78:81], v[154:157], v[214:217]
	v_mov_b32_e32 v184, v246
	v_mov_b32_e32 v185, v247
	buffer_load_dwordx2 v[194:195], v209, s[20:23], s45 offen
	s_add_i32 s40, s40, 1
	s_add_i32 s44, s44, 0x1000
	s_waitcnt lgkmcnt(0)
	s_barrier
	ds_read_b128 v[158:161], v248 offset:0
	ds_read_b128 v[162:165], v248 offset:1024
	ds_read_b128 v[166:169], v249 offset:2048
	ds_read_b128 v[170:173], v249 offset:3072
	v_mfma_f32_16x16x32_f16 v[218:221], v[82:85], v[150:153], v[106:109]
	v_mfma_f32_16x16x32_f16 v[222:225], v[90:93], v[150:153], v[110:113]
	v_mfma_f32_16x16x32_f16 v[218:221], v[86:89], v[154:157], v[218:221]
	v_mfma_f32_16x16x32_f16 v[222:225], v[94:97], v[154:157], v[222:225]
	s_waitcnt lgkmcnt(2)
	v_mfma_f32_16x16x32_f16 v[210:213], v[54:57], v[158:161], v[210:213]
	v_mfma_f32_16x16x32_f16 v[210:213], v[58:61], v[162:165], v[210:213]
	s_waitcnt lgkmcnt(0)
	v_mfma_f32_16x16x32_f16 v[210:213], v[62:65], v[166:169], v[210:213]
	v_mfma_f32_16x16x32_f16 v[210:213], v[50:53], v[170:173], v[210:213]
	s_waitcnt vmcnt(9)
	v_cvt_pk_f16_f32 v251, v192, v193
	ds_write_b32 v1, v251 offset:0
	ds_read_b128 v[150:153], v186 offset:6144
	ds_read_b128 v[154:157], v186 offset:7168
	s_add_i32 s45, s45, 0x100000
	s_add_i32 s46, s46, 0x4000
	s_movk_i32 s47, 0x0
	s_add_i32 s43, s40, -12
	s_lshl_b32 s43, s43, 12
	s_cmp_lt_u32 s40, 14
	s_cselect_b32 s43, s47, s43
	v_exp_f32_e32 v226, v210
	v_exp_f32_e32 v227, v211
	v_mfma_f32_16x16x32_f16 v[214:217], v[34:37], v[158:161], v[214:217]
	v_min_f32_e32 v228, s42, v212
	v_exp_f32_e32 v229, v213
	v_mfma_f32_16x16x32_f16 v[214:217], v[38:41], v[162:165], v[214:217]
	v_exp_f32_e32 v228, v228
	v_add_f32_e32 v227, 1.0, v227
	v_mfma_f32_16x16x32_f16 v[214:217], v[42:45], v[166:169], v[214:217]
	v_fma_f32 v230, v228, s41, s41
	v_rcp_f32_e32 v227, v227
	v_mfma_f32_16x16x32_f16 v[214:217], v[46:49], v[170:173], v[214:217]
	v_fma_f32 v230, v226, v230, v230
	v_rcp_f32_e32 v230, v230
	v_mfma_f32_16x16x32_f16 v[218:221], v[18:21], v[158:161], v[218:221]
	v_fma_f32 v226, -v228, v230, v230
	v_fma_f32 v200, v200, v227, v226
	v_mfma_f32_16x16x32_f16 v[218:221], v[14:17], v[162:165], v[218:221]
	v_min_f32_e32 v226, s42, v200
	v_exp_f32_e32 v226, v226
	v_mfma_f32_16x16x32_f16 v[218:221], v[10:13], v[166:169], v[218:221]
	v_add_f32_e32 v227, 1.0, v226
	v_fma_f32 v227, v229, v227, v227
	v_mfma_f32_16x16x32_f16 v[218:221], v[26:29], v[170:173], v[218:221]
	v_rcp_f32_e32 v227, v227
	v_exp_f32_e32 v231, v214
	v_mfma_f32_16x16x32_f16 v[222:225], v[2:5], v[158:161], v[222:225]
	v_exp_f32_e32 v232, v215
	v_fma_f32 v226, -v226, v227, v227
	v_mfma_f32_16x16x32_f16 v[222:225], v[6:9], v[162:165], v[222:225]
	v_min_f32_e32 v233, s42, v216
	v_exp_f32_e32 v234, v217
	v_mfma_f32_16x16x32_f16 v[222:225], v[22:25], v[166:169], v[222:225]
	v_exp_f32_e32 v236, v218
	v_exp_f32_e32 v233, v233
	v_mfma_f32_16x16x32_f16 v[222:225], v[30:33], v[170:173], v[222:225]
	v_add_f32_e32 v232, 1.0, v232
	v_exp_f32_e32 v227, v219
	v_fma_f32 v235, v233, s41, s41
	v_rcp_f32_e32 v232, v232
	v_min_f32_e32 v228, s42, v220
	v_fma_f32 v235, v231, v235, v235
	v_rcp_f32_e32 v235, v235
	v_exp_f32_e32 v229, v221
	v_fma_f32 v231, -v233, v235, v235
	v_fma_f32 v201, v201, v232, v231
	v_exp_f32_e32 v228, v228
	v_min_f32_e32 v231, s42, v201
	v_exp_f32_e32 v231, v231
	v_add_f32_e32 v227, 1.0, v227
	v_add_f32_e32 v232, 1.0, v231
	v_mfma_f32_16x16x32_f16 v[146:149], v[122:125], v[158:161], v[146:149]
	v_fma_f32 v232, v234, v232, v232
	v_fma_f32 v230, v228, s41, s41
	v_rcp_f32_e32 v232, v232
	v_mfma_f32_16x16x32_f16 v[146:149], v[126:129], v[162:165], v[146:149]
	v_fma_f32 v231, -v231, v232, v232
	v_rcp_f32_e32 v227, v227
	v_cvt_pk_f16_f32 v246, v226, v231
	buffer_load_dwordx4 v[122:125], v189, s[16:19], s46 offen
	buffer_load_dwordx4 v[126:129], v208, s[16:19], s46 offen
	v_exp_f32_e32 v231, v222
	v_fma_f32 v230, v236, v230, v230
	v_exp_f32_e32 v232, v223
	s_waitcnt lgkmcnt(0)
	v_mfma_f32_16x16x32_f16 v[210:213], v[70:73], v[150:153], v[98:101]
	v_min_f32_e32 v233, s42, v224
	v_rcp_f32_e32 v230, v230
	v_exp_f32_e32 v234, v225
	v_mfma_f32_16x16x32_f16 v[214:217], v[74:77], v[150:153], v[102:105]
	v_exp_f32_e32 v233, v233
	v_fma_f32 v236, -v228, v230, v230
	v_add_f32_e32 v232, 1.0, v232
	v_fma_f32 v235, v233, s41, s41
	v_fma_f32 v198, v198, v227, v236
	v_rcp_f32_e32 v232, v232
	v_fma_f32 v235, v231, v235, v235
	v_min_f32_e32 v236, s42, v198
	v_rcp_f32_e32 v235, v235
	s_nop 0
	v_fma_f32 v231, -v233, v235, v235
	v_exp_f32_e32 v236, v236
	v_fma_f32 v199, v199, v232, v231
	v_min_f32_e32 v231, s42, v199
	v_add_f32_e32 v227, 1.0, v236
	v_exp_f32_e32 v231, v231
	v_fma_f32 v227, v229, v227, v227
	v_add_u32_e32 v250, s43, v206
	v_add_f32_e32 v232, 1.0, v231
	v_rcp_f32_e32 v227, v227
	v_add_u32_e32 v248, s43, v252
	v_fma_f32 v232, v234, v232, v232
	v_fma_f32 v236, -v236, v227, v227
	v_add_u32_e32 v249, s43, v253
	v_rcp_f32_e32 v232, v232
	s_nop 0
	v_fma_f32 v231, -v231, v232, v232
	v_cvt_pk_f16_f32 v247, v236, v231
	ds_write_b64 v250, v[246:247] offset:8192
	v_mfma_f32_16x16x32_f16 v[210:213], v[66:69], v[154:157], v[210:213]
	v_mfma_f32_16x16x32_f16 v[214:217], v[78:81], v[154:157], v[214:217]
	v_mov_b32_e32 v237, v246
	v_mov_b32_e32 v238, v247
	buffer_load_dwordx2 v[192:193], v209, s[20:23], s45 offen
	s_add_i32 s40, s40, 1
	s_add_i32 s44, s44, 0x1000
	s_waitcnt lgkmcnt(0)
	s_barrier
	ds_read_b128 v[158:161], v248 offset:0
	ds_read_b128 v[162:165], v248 offset:1024
	ds_read_b128 v[166:169], v249 offset:2048
	ds_read_b128 v[170:173], v249 offset:3072
	v_mfma_f32_16x16x32_f16 v[218:221], v[82:85], v[150:153], v[106:109]
	v_mfma_f32_16x16x32_f16 v[222:225], v[90:93], v[150:153], v[110:113]
	v_mfma_f32_16x16x32_f16 v[218:221], v[86:89], v[154:157], v[218:221]
	v_mfma_f32_16x16x32_f16 v[222:225], v[94:97], v[154:157], v[222:225]
	s_waitcnt lgkmcnt(2)
	v_mfma_f32_16x16x32_f16 v[210:213], v[54:57], v[158:161], v[210:213]
	v_mfma_f32_16x16x32_f16 v[210:213], v[58:61], v[162:165], v[210:213]
	s_waitcnt lgkmcnt(0)
	v_mfma_f32_16x16x32_f16 v[210:213], v[62:65], v[166:169], v[210:213]
	v_mfma_f32_16x16x32_f16 v[210:213], v[50:53], v[170:173], v[210:213]
	s_waitcnt vmcnt(9)
	v_cvt_pk_f16_f32 v251, v190, v191
	ds_write_b32 v1, v251 offset:2048
	ds_read_b128 v[150:153], v186 offset:0
	ds_read_b128 v[154:157], v186 offset:1024
	s_add_i32 s45, s45, 0x100000
	s_add_i32 s46, s46, 0x4000
	s_movk_i32 s47, 0x1000
	s_add_i32 s43, s40, -12
	s_lshl_b32 s43, s43, 12
	s_cmp_lt_u32 s40, 14
	s_cselect_b32 s43, s47, s43
	v_exp_f32_e32 v226, v210
	v_exp_f32_e32 v227, v211
	v_mfma_f32_16x16x32_f16 v[214:217], v[34:37], v[158:161], v[214:217]
	v_min_f32_e32 v228, s42, v212
	v_exp_f32_e32 v229, v213
	v_mfma_f32_16x16x32_f16 v[214:217], v[38:41], v[162:165], v[214:217]
	v_exp_f32_e32 v228, v228
	v_add_f32_e32 v227, 1.0, v227
	v_mfma_f32_16x16x32_f16 v[214:217], v[42:45], v[166:169], v[214:217]
	v_fma_f32 v230, v228, s41, s41
	v_rcp_f32_e32 v227, v227
	v_mfma_f32_16x16x32_f16 v[214:217], v[46:49], v[170:173], v[214:217]
	v_fma_f32 v230, v226, v230, v230
	v_rcp_f32_e32 v230, v230
	v_mfma_f32_16x16x32_f16 v[218:221], v[18:21], v[158:161], v[218:221]
	v_fma_f32 v226, -v228, v230, v230
	v_fma_f32 v200, v200, v227, v226
	v_mfma_f32_16x16x32_f16 v[218:221], v[14:17], v[162:165], v[218:221]
	v_min_f32_e32 v226, s42, v200
	v_exp_f32_e32 v226, v226
	v_mfma_f32_16x16x32_f16 v[218:221], v[10:13], v[166:169], v[218:221]
	v_add_f32_e32 v227, 1.0, v226
	v_fma_f32 v227, v229, v227, v227
	v_mfma_f32_16x16x32_f16 v[218:221], v[26:29], v[170:173], v[218:221]
	v_rcp_f32_e32 v227, v227
	v_exp_f32_e32 v231, v214
	v_mfma_f32_16x16x32_f16 v[222:225], v[2:5], v[158:161], v[222:225]
	v_exp_f32_e32 v232, v215
	v_fma_f32 v226, -v226, v227, v227
	v_mfma_f32_16x16x32_f16 v[222:225], v[6:9], v[162:165], v[222:225]
	v_min_f32_e32 v233, s42, v216
	v_exp_f32_e32 v234, v217
	v_mfma_f32_16x16x32_f16 v[222:225], v[22:25], v[166:169], v[222:225]
	v_exp_f32_e32 v236, v218
	v_exp_f32_e32 v233, v233
	v_mfma_f32_16x16x32_f16 v[222:225], v[30:33], v[170:173], v[222:225]
	v_add_f32_e32 v232, 1.0, v232
	v_exp_f32_e32 v227, v219
	v_fma_f32 v235, v233, s41, s41
	v_rcp_f32_e32 v232, v232
	v_min_f32_e32 v228, s42, v220
	v_fma_f32 v235, v231, v235, v235
	v_rcp_f32_e32 v235, v235
	v_exp_f32_e32 v229, v221
	v_fma_f32 v231, -v233, v235, v235
	v_fma_f32 v201, v201, v232, v231
	v_exp_f32_e32 v228, v228
	v_min_f32_e32 v231, s42, v201
	v_exp_f32_e32 v231, v231
	v_add_f32_e32 v227, 1.0, v227
	v_add_f32_e32 v232, 1.0, v231
	v_mfma_f32_16x16x32_f16 v[146:149], v[114:117], v[158:161], v[146:149]
	v_fma_f32 v232, v234, v232, v232
	v_fma_f32 v230, v228, s41, s41
	v_rcp_f32_e32 v232, v232
	v_mfma_f32_16x16x32_f16 v[146:149], v[118:121], v[162:165], v[146:149]
	v_fma_f32 v231, -v231, v232, v232
	v_rcp_f32_e32 v227, v227
	v_cvt_pk_f16_f32 v246, v226, v231
	buffer_load_dwordx4 v[114:117], v189, s[16:19], s46 offen
	buffer_load_dwordx4 v[118:121], v208, s[16:19], s46 offen
	v_exp_f32_e32 v231, v222
	v_fma_f32 v230, v236, v230, v230
	v_exp_f32_e32 v232, v223
	s_waitcnt lgkmcnt(0)
	v_mfma_f32_16x16x32_f16 v[210:213], v[70:73], v[150:153], v[98:101]
	v_min_f32_e32 v233, s42, v224
	v_rcp_f32_e32 v230, v230
	v_exp_f32_e32 v234, v225
	v_mfma_f32_16x16x32_f16 v[214:217], v[74:77], v[150:153], v[102:105]
	v_exp_f32_e32 v233, v233
	v_fma_f32 v236, -v228, v230, v230
	v_add_f32_e32 v232, 1.0, v232
	v_fma_f32 v235, v233, s41, s41
	v_fma_f32 v198, v198, v227, v236
	v_rcp_f32_e32 v232, v232
	v_fma_f32 v235, v231, v235, v235
	v_min_f32_e32 v236, s42, v198
	v_rcp_f32_e32 v235, v235
	s_nop 0
	v_fma_f32 v231, -v233, v235, v235
	v_exp_f32_e32 v236, v236
	v_fma_f32 v199, v199, v232, v231
	v_min_f32_e32 v231, s42, v199
	v_add_f32_e32 v227, 1.0, v236
	v_exp_f32_e32 v231, v231
	v_fma_f32 v227, v229, v227, v227
	v_add_u32_e32 v250, s43, v206
	v_add_f32_e32 v232, 1.0, v231
	v_rcp_f32_e32 v227, v227
	v_add_u32_e32 v248, s43, v252
	v_fma_f32 v232, v234, v232, v232
	v_fma_f32 v236, -v236, v227, v227
	v_add_u32_e32 v249, s43, v253
	v_rcp_f32_e32 v232, v232
	s_nop 0
	v_fma_f32 v231, -v231, v232, v232
	v_cvt_pk_f16_f32 v247, v236, v231
	ds_write_b64 v250, v[246:247] offset:8192
	v_mfma_f32_16x16x32_f16 v[210:213], v[66:69], v[154:157], v[210:213]
	v_mfma_f32_16x16x32_f16 v[214:217], v[78:81], v[154:157], v[214:217]
	v_mov_b32_e32 v239, v246
	v_mov_b32_e32 v240, v247
	buffer_load_dwordx2 v[190:191], v209, s[20:23], s45 offen
	s_add_i32 s40, s40, 1
	s_add_i32 s44, s44, 0x1000
	s_waitcnt lgkmcnt(0)
	s_barrier
	ds_read_b128 v[158:161], v248 offset:0
	ds_read_b128 v[162:165], v248 offset:1024
	ds_read_b128 v[166:169], v249 offset:2048
	ds_read_b128 v[170:173], v249 offset:3072
	v_mfma_f32_16x16x32_f16 v[218:221], v[82:85], v[150:153], v[106:109]
	v_mfma_f32_16x16x32_f16 v[222:225], v[90:93], v[150:153], v[110:113]
	v_mfma_f32_16x16x32_f16 v[218:221], v[86:89], v[154:157], v[218:221]
	v_mfma_f32_16x16x32_f16 v[222:225], v[94:97], v[154:157], v[222:225]
	s_waitcnt lgkmcnt(2)
	v_mfma_f32_16x16x32_f16 v[210:213], v[54:57], v[158:161], v[210:213]
	v_mfma_f32_16x16x32_f16 v[210:213], v[58:61], v[162:165], v[210:213]
	s_waitcnt lgkmcnt(0)
	v_mfma_f32_16x16x32_f16 v[210:213], v[62:65], v[166:169], v[210:213]
	v_mfma_f32_16x16x32_f16 v[210:213], v[50:53], v[170:173], v[210:213]
	s_waitcnt vmcnt(9)
	v_cvt_pk_f16_f32 v251, v196, v197
	ds_write_b32 v1, v251 offset:4096
	ds_read_b128 v[150:153], v186 offset:2048
	ds_read_b128 v[154:157], v186 offset:3072
	s_add_i32 s45, s45, 0x100000
	s_add_i32 s46, s46, 0x4000
	s_movk_i32 s47, 0x0
	s_add_i32 s43, s40, -12
	s_lshl_b32 s43, s43, 12
	s_cmp_lt_u32 s40, 14
	s_cselect_b32 s43, s47, s43
	v_exp_f32_e32 v226, v210
	v_exp_f32_e32 v227, v211
	v_mfma_f32_16x16x32_f16 v[214:217], v[34:37], v[158:161], v[214:217]
	v_min_f32_e32 v228, s42, v212
	v_exp_f32_e32 v229, v213
	v_mfma_f32_16x16x32_f16 v[214:217], v[38:41], v[162:165], v[214:217]
	v_exp_f32_e32 v228, v228
	v_add_f32_e32 v227, 1.0, v227
	v_mfma_f32_16x16x32_f16 v[214:217], v[42:45], v[166:169], v[214:217]
	v_fma_f32 v230, v228, s41, s41
	v_rcp_f32_e32 v227, v227
	v_mfma_f32_16x16x32_f16 v[214:217], v[46:49], v[170:173], v[214:217]
	v_fma_f32 v230, v226, v230, v230
	v_rcp_f32_e32 v230, v230
	v_mfma_f32_16x16x32_f16 v[218:221], v[18:21], v[158:161], v[218:221]
	v_fma_f32 v226, -v228, v230, v230
	v_fma_f32 v200, v200, v227, v226
	v_mfma_f32_16x16x32_f16 v[218:221], v[14:17], v[162:165], v[218:221]
	v_min_f32_e32 v226, s42, v200
	v_exp_f32_e32 v226, v226
	v_mfma_f32_16x16x32_f16 v[218:221], v[10:13], v[166:169], v[218:221]
	v_add_f32_e32 v227, 1.0, v226
	v_fma_f32 v227, v229, v227, v227
	v_mfma_f32_16x16x32_f16 v[218:221], v[26:29], v[170:173], v[218:221]
	v_rcp_f32_e32 v227, v227
	v_exp_f32_e32 v231, v214
	v_mfma_f32_16x16x32_f16 v[222:225], v[2:5], v[158:161], v[222:225]
	v_exp_f32_e32 v232, v215
	v_fma_f32 v226, -v226, v227, v227
	v_mfma_f32_16x16x32_f16 v[222:225], v[6:9], v[162:165], v[222:225]
	v_min_f32_e32 v233, s42, v216
	v_exp_f32_e32 v234, v217
	v_mfma_f32_16x16x32_f16 v[222:225], v[22:25], v[166:169], v[222:225]
	v_exp_f32_e32 v236, v218
	v_exp_f32_e32 v233, v233
	v_mfma_f32_16x16x32_f16 v[222:225], v[30:33], v[170:173], v[222:225]
	v_add_f32_e32 v232, 1.0, v232
	v_exp_f32_e32 v227, v219
	v_fma_f32 v235, v233, s41, s41
	v_rcp_f32_e32 v232, v232
	v_min_f32_e32 v228, s42, v220
	v_fma_f32 v235, v231, v235, v235
	v_rcp_f32_e32 v235, v235
	v_exp_f32_e32 v229, v221
	v_fma_f32 v231, -v233, v235, v235
	v_fma_f32 v201, v201, v232, v231
	v_exp_f32_e32 v228, v228
	v_min_f32_e32 v231, s42, v201
	v_exp_f32_e32 v231, v231
	v_add_f32_e32 v227, 1.0, v227
	v_add_f32_e32 v232, 1.0, v231
	v_mfma_f32_16x16x32_f16 v[146:149], v[138:141], v[158:161], v[146:149]
	v_fma_f32 v232, v234, v232, v232
	v_fma_f32 v230, v228, s41, s41
	v_rcp_f32_e32 v232, v232
	v_mfma_f32_16x16x32_f16 v[146:149], v[142:145], v[162:165], v[146:149]
	v_fma_f32 v231, -v231, v232, v232
	v_rcp_f32_e32 v227, v227
	v_cvt_pk_f16_f32 v246, v226, v231
	buffer_load_dwordx4 v[138:141], v189, s[16:19], s46 offen
	buffer_load_dwordx4 v[142:145], v208, s[16:19], s46 offen
	v_exp_f32_e32 v231, v222
	v_fma_f32 v230, v236, v230, v230
	v_exp_f32_e32 v232, v223
	s_waitcnt lgkmcnt(0)
	v_mfma_f32_16x16x32_f16 v[210:213], v[70:73], v[150:153], v[98:101]
	v_min_f32_e32 v233, s42, v224
	v_rcp_f32_e32 v230, v230
	v_exp_f32_e32 v234, v225
	v_mfma_f32_16x16x32_f16 v[214:217], v[74:77], v[150:153], v[102:105]
	v_exp_f32_e32 v233, v233
	v_fma_f32 v236, -v228, v230, v230
	v_add_f32_e32 v232, 1.0, v232
	v_fma_f32 v235, v233, s41, s41
	v_fma_f32 v198, v198, v227, v236
	v_rcp_f32_e32 v232, v232
	v_fma_f32 v235, v231, v235, v235
	v_min_f32_e32 v236, s42, v198
	v_rcp_f32_e32 v235, v235
	s_nop 0
	v_fma_f32 v231, -v233, v235, v235
	v_exp_f32_e32 v236, v236
	v_fma_f32 v199, v199, v232, v231
	v_min_f32_e32 v231, s42, v199
	v_add_f32_e32 v227, 1.0, v236
	v_exp_f32_e32 v231, v231
	v_fma_f32 v227, v229, v227, v227
	v_add_u32_e32 v250, s43, v206
	v_add_f32_e32 v232, 1.0, v231
	v_rcp_f32_e32 v227, v227
	v_add_u32_e32 v248, s43, v252
	v_fma_f32 v232, v234, v232, v232
	v_fma_f32 v236, -v236, v227, v227
	v_add_u32_e32 v249, s43, v253
	v_rcp_f32_e32 v232, v232
	s_nop 0
	v_fma_f32 v231, -v231, v232, v232
	v_cvt_pk_f16_f32 v247, v236, v231
	ds_write_b64 v250, v[246:247] offset:8192
	v_mfma_f32_16x16x32_f16 v[210:213], v[66:69], v[154:157], v[210:213]
	v_mfma_f32_16x16x32_f16 v[214:217], v[78:81], v[154:157], v[214:217]
	v_mov_b32_e32 v241, v246
	v_mov_b32_e32 v242, v247
	buffer_load_dwordx2 v[196:197], v209, s[20:23], s45 offen
	s_add_i32 s40, s40, 1
	s_add_i32 s44, s44, 0x1000
	s_waitcnt lgkmcnt(0)
	s_barrier
	ds_read_b128 v[158:161], v248 offset:0
	ds_read_b128 v[162:165], v248 offset:1024
	ds_read_b128 v[166:169], v249 offset:2048
	ds_read_b128 v[170:173], v249 offset:3072
	v_mfma_f32_16x16x32_f16 v[218:221], v[82:85], v[150:153], v[106:109]
	v_mfma_f32_16x16x32_f16 v[222:225], v[90:93], v[150:153], v[110:113]
	v_mfma_f32_16x16x32_f16 v[218:221], v[86:89], v[154:157], v[218:221]
	v_mfma_f32_16x16x32_f16 v[222:225], v[94:97], v[154:157], v[222:225]
	s_waitcnt lgkmcnt(2)
	v_mfma_f32_16x16x32_f16 v[210:213], v[54:57], v[158:161], v[210:213]
	v_mfma_f32_16x16x32_f16 v[210:213], v[58:61], v[162:165], v[210:213]
	s_waitcnt lgkmcnt(0)
	v_mfma_f32_16x16x32_f16 v[210:213], v[62:65], v[166:169], v[210:213]
	v_mfma_f32_16x16x32_f16 v[210:213], v[50:53], v[170:173], v[210:213]
	s_waitcnt vmcnt(9)
	v_cvt_pk_f16_f32 v251, v194, v195
	ds_write_b32 v1, v251 offset:6144
	ds_read_b128 v[150:153], v186 offset:4096
	ds_read_b128 v[154:157], v186 offset:5120
	s_add_i32 s45, s45, 0x100000
	s_add_i32 s46, s46, 0x4000
	s_movk_i32 s47, 0x1000
	s_add_i32 s43, s40, -12
	s_lshl_b32 s43, s43, 12
	s_cmp_lt_u32 s40, 14
	s_cselect_b32 s43, s47, s43
	v_exp_f32_e32 v226, v210
	v_exp_f32_e32 v227, v211
	v_mfma_f32_16x16x32_f16 v[214:217], v[34:37], v[158:161], v[214:217]
	v_min_f32_e32 v228, s42, v212
	v_exp_f32_e32 v229, v213
	v_mfma_f32_16x16x32_f16 v[214:217], v[38:41], v[162:165], v[214:217]
	v_exp_f32_e32 v228, v228
	v_add_f32_e32 v227, 1.0, v227
	v_mfma_f32_16x16x32_f16 v[214:217], v[42:45], v[166:169], v[214:217]
	v_fma_f32 v230, v228, s41, s41
	v_rcp_f32_e32 v227, v227
	v_mfma_f32_16x16x32_f16 v[214:217], v[46:49], v[170:173], v[214:217]
	v_fma_f32 v230, v226, v230, v230
	v_rcp_f32_e32 v230, v230
	v_mfma_f32_16x16x32_f16 v[218:221], v[18:21], v[158:161], v[218:221]
	v_fma_f32 v226, -v228, v230, v230
	v_fma_f32 v200, v200, v227, v226
	v_mfma_f32_16x16x32_f16 v[218:221], v[14:17], v[162:165], v[218:221]
	v_min_f32_e32 v226, s42, v200
	v_exp_f32_e32 v226, v226
	v_mfma_f32_16x16x32_f16 v[218:221], v[10:13], v[166:169], v[218:221]
	v_add_f32_e32 v227, 1.0, v226
	v_fma_f32 v227, v229, v227, v227
	v_mfma_f32_16x16x32_f16 v[218:221], v[26:29], v[170:173], v[218:221]
	v_rcp_f32_e32 v227, v227
	v_exp_f32_e32 v231, v214
	v_mfma_f32_16x16x32_f16 v[222:225], v[2:5], v[158:161], v[222:225]
	v_exp_f32_e32 v232, v215
	v_fma_f32 v226, -v226, v227, v227
	v_mfma_f32_16x16x32_f16 v[222:225], v[6:9], v[162:165], v[222:225]
	v_min_f32_e32 v233, s42, v216
	v_exp_f32_e32 v234, v217
	v_mfma_f32_16x16x32_f16 v[222:225], v[22:25], v[166:169], v[222:225]
	v_exp_f32_e32 v236, v218
	v_exp_f32_e32 v233, v233
	v_mfma_f32_16x16x32_f16 v[222:225], v[30:33], v[170:173], v[222:225]
	v_add_f32_e32 v232, 1.0, v232
	v_exp_f32_e32 v227, v219
	v_fma_f32 v235, v233, s41, s41
	v_rcp_f32_e32 v232, v232
	v_min_f32_e32 v228, s42, v220
	v_fma_f32 v235, v231, v235, v235
	v_rcp_f32_e32 v235, v235
	v_exp_f32_e32 v229, v221
	v_fma_f32 v231, -v233, v235, v235
	v_fma_f32 v201, v201, v232, v231
	v_exp_f32_e32 v228, v228
	v_min_f32_e32 v231, s42, v201
	v_exp_f32_e32 v231, v231
	v_add_f32_e32 v227, 1.0, v227
	v_add_f32_e32 v232, 1.0, v231
	v_mfma_f32_16x16x32_f16 v[146:149], v[130:133], v[158:161], v[146:149]
	v_fma_f32 v232, v234, v232, v232
	v_fma_f32 v230, v228, s41, s41
	v_rcp_f32_e32 v232, v232
	v_mfma_f32_16x16x32_f16 v[146:149], v[134:137], v[162:165], v[146:149]
	v_fma_f32 v231, -v231, v232, v232
	v_rcp_f32_e32 v227, v227
	v_cvt_pk_f16_f32 v246, v226, v231
	buffer_load_dwordx4 v[130:133], v189, s[16:19], s46 offen
	buffer_load_dwordx4 v[134:137], v208, s[16:19], s46 offen
	v_exp_f32_e32 v231, v222
	v_fma_f32 v230, v236, v230, v230
	v_exp_f32_e32 v232, v223
	s_waitcnt lgkmcnt(0)
	v_mfma_f32_16x16x32_f16 v[210:213], v[70:73], v[150:153], v[98:101]
	v_min_f32_e32 v233, s42, v224
	v_rcp_f32_e32 v230, v230
	v_exp_f32_e32 v234, v225
	v_mfma_f32_16x16x32_f16 v[214:217], v[74:77], v[150:153], v[102:105]
	v_exp_f32_e32 v233, v233
	v_fma_f32 v236, -v228, v230, v230
	v_add_f32_e32 v232, 1.0, v232
	v_fma_f32 v235, v233, s41, s41
	v_fma_f32 v198, v198, v227, v236
	v_rcp_f32_e32 v232, v232
	v_fma_f32 v235, v231, v235, v235
	v_min_f32_e32 v236, s42, v198
	v_rcp_f32_e32 v235, v235
	s_nop 0
	v_fma_f32 v231, -v233, v235, v235
	v_exp_f32_e32 v236, v236
	v_fma_f32 v199, v199, v232, v231
	v_min_f32_e32 v231, s42, v199
	v_add_f32_e32 v227, 1.0, v236
	v_exp_f32_e32 v231, v231
	v_fma_f32 v227, v229, v227, v227
	v_add_u32_e32 v250, s43, v206
	v_add_f32_e32 v232, 1.0, v231
	v_rcp_f32_e32 v227, v227
	v_add_u32_e32 v248, s43, v252
	v_fma_f32 v232, v234, v232, v232
	v_fma_f32 v236, -v236, v227, v227
	v_add_u32_e32 v249, s43, v253
	v_rcp_f32_e32 v232, v232
	s_nop 0
	v_fma_f32 v231, -v231, v232, v232
	v_cvt_pk_f16_f32 v247, v236, v231
	ds_write_b64 v250, v[246:247] offset:8192
	v_mfma_f32_16x16x32_f16 v[210:213], v[66:69], v[154:157], v[210:213]
	v_mfma_f32_16x16x32_f16 v[214:217], v[78:81], v[154:157], v[214:217]
	v_mov_b32_e32 v243, v246
	v_mov_b32_e32 v244, v247
	buffer_load_dwordx2 v[194:195], v209, s[20:23], s45 offen
	s_add_i32 s40, s40, 1
	s_add_i32 s44, s44, 0x1000
	s_waitcnt lgkmcnt(0)
	s_barrier
	ds_read_b128 v[158:161], v248 offset:0
	ds_read_b128 v[162:165], v248 offset:1024
	ds_read_b128 v[166:169], v249 offset:2048
	ds_read_b128 v[170:173], v249 offset:3072
	v_mfma_f32_16x16x32_f16 v[218:221], v[82:85], v[150:153], v[106:109]
	v_mfma_f32_16x16x32_f16 v[222:225], v[90:93], v[150:153], v[110:113]
	v_mfma_f32_16x16x32_f16 v[218:221], v[86:89], v[154:157], v[218:221]
	v_mfma_f32_16x16x32_f16 v[222:225], v[94:97], v[154:157], v[222:225]
	s_waitcnt lgkmcnt(2)
	v_mfma_f32_16x16x32_f16 v[210:213], v[54:57], v[158:161], v[210:213]
	v_mfma_f32_16x16x32_f16 v[210:213], v[58:61], v[162:165], v[210:213]
	s_waitcnt lgkmcnt(0)
	v_mfma_f32_16x16x32_f16 v[210:213], v[62:65], v[166:169], v[210:213]
	v_mfma_f32_16x16x32_f16 v[210:213], v[50:53], v[170:173], v[210:213]
	s_waitcnt vmcnt(9)
	v_cvt_pk_f16_f32 v251, v192, v193
	ds_write_b32 v1, v251 offset:0
	ds_read_b128 v[150:153], v186 offset:6144
	ds_read_b128 v[154:157], v186 offset:7168
	s_add_i32 s45, s45, 0x100000
	s_add_i32 s46, s46, 0x4000
	s_movk_i32 s47, 0x0
	s_add_i32 s43, s40, -12
	s_lshl_b32 s43, s43, 12
	s_cmp_lt_u32 s40, 14
	s_cselect_b32 s43, s47, s43
	v_exp_f32_e32 v226, v210
	v_exp_f32_e32 v227, v211
	v_mfma_f32_16x16x32_f16 v[214:217], v[34:37], v[158:161], v[214:217]
	v_min_f32_e32 v228, s42, v212
	v_exp_f32_e32 v229, v213
	v_mfma_f32_16x16x32_f16 v[214:217], v[38:41], v[162:165], v[214:217]
	v_exp_f32_e32 v228, v228
	v_add_f32_e32 v227, 1.0, v227
	v_mfma_f32_16x16x32_f16 v[214:217], v[42:45], v[166:169], v[214:217]
	v_fma_f32 v230, v228, s41, s41
	v_rcp_f32_e32 v227, v227
	v_mfma_f32_16x16x32_f16 v[214:217], v[46:49], v[170:173], v[214:217]
	v_fma_f32 v230, v226, v230, v230
	v_rcp_f32_e32 v230, v230
	v_mfma_f32_16x16x32_f16 v[218:221], v[18:21], v[158:161], v[218:221]
	v_fma_f32 v226, -v228, v230, v230
	v_fma_f32 v200, v200, v227, v226
	v_mfma_f32_16x16x32_f16 v[218:221], v[14:17], v[162:165], v[218:221]
	v_min_f32_e32 v226, s42, v200
	v_exp_f32_e32 v226, v226
	v_mfma_f32_16x16x32_f16 v[218:221], v[10:13], v[166:169], v[218:221]
	v_add_f32_e32 v227, 1.0, v226
	v_fma_f32 v227, v229, v227, v227
	v_mfma_f32_16x16x32_f16 v[218:221], v[26:29], v[170:173], v[218:221]
	v_rcp_f32_e32 v227, v227
	v_exp_f32_e32 v231, v214
	v_mfma_f32_16x16x32_f16 v[222:225], v[2:5], v[158:161], v[222:225]
	v_exp_f32_e32 v232, v215
	v_fma_f32 v226, -v226, v227, v227
	v_mfma_f32_16x16x32_f16 v[222:225], v[6:9], v[162:165], v[222:225]
	v_min_f32_e32 v233, s42, v216
	v_exp_f32_e32 v234, v217
	v_mfma_f32_16x16x32_f16 v[222:225], v[22:25], v[166:169], v[222:225]
	v_exp_f32_e32 v236, v218
	v_exp_f32_e32 v233, v233
	v_mfma_f32_16x16x32_f16 v[222:225], v[30:33], v[170:173], v[222:225]
	v_add_f32_e32 v232, 1.0, v232
	v_exp_f32_e32 v227, v219
	v_fma_f32 v235, v233, s41, s41
	v_rcp_f32_e32 v232, v232
	v_min_f32_e32 v228, s42, v220
	v_fma_f32 v235, v231, v235, v235
	v_rcp_f32_e32 v235, v235
	v_exp_f32_e32 v229, v221
	v_fma_f32 v231, -v233, v235, v235
	v_fma_f32 v201, v201, v232, v231
	v_exp_f32_e32 v228, v228
	v_min_f32_e32 v231, s42, v201
	v_exp_f32_e32 v231, v231
	v_add_f32_e32 v227, 1.0, v227
	v_add_f32_e32 v232, 1.0, v231
	v_mfma_f32_16x16x32_f16 v[146:149], v[122:125], v[158:161], v[146:149]
	v_fma_f32 v232, v234, v232, v232
	v_fma_f32 v230, v228, s41, s41
	v_rcp_f32_e32 v232, v232
	v_mfma_f32_16x16x32_f16 v[146:149], v[126:129], v[162:165], v[146:149]
	v_fma_f32 v231, -v231, v232, v232
	v_rcp_f32_e32 v227, v227
	v_cvt_pk_f16_f32 v246, v226, v231
	buffer_load_dwordx4 v[122:125], v189, s[16:19], s46 offen
	buffer_load_dwordx4 v[126:129], v208, s[16:19], s46 offen
	v_exp_f32_e32 v231, v222
	v_fma_f32 v230, v236, v230, v230
	v_exp_f32_e32 v232, v223
	s_waitcnt lgkmcnt(0)
	v_mfma_f32_16x16x32_f16 v[210:213], v[70:73], v[150:153], v[98:101]
	v_min_f32_e32 v233, s42, v224
	v_rcp_f32_e32 v230, v230
	v_exp_f32_e32 v234, v225
	v_mfma_f32_16x16x32_f16 v[214:217], v[74:77], v[150:153], v[102:105]
	v_exp_f32_e32 v233, v233
	v_fma_f32 v236, -v228, v230, v230
	v_add_f32_e32 v232, 1.0, v232
	v_fma_f32 v235, v233, s41, s41
	v_fma_f32 v198, v198, v227, v236
	v_rcp_f32_e32 v232, v232
	v_fma_f32 v235, v231, v235, v235
	v_min_f32_e32 v236, s42, v198
	v_rcp_f32_e32 v235, v235
	s_nop 0
	v_fma_f32 v231, -v233, v235, v235
	v_exp_f32_e32 v236, v236
	v_fma_f32 v199, v199, v232, v231
	v_min_f32_e32 v231, s42, v199
	v_add_f32_e32 v227, 1.0, v236
	v_exp_f32_e32 v231, v231
	v_fma_f32 v227, v229, v227, v227
	v_add_u32_e32 v250, s43, v206
	v_add_f32_e32 v232, 1.0, v231
	v_rcp_f32_e32 v227, v227
	v_add_u32_e32 v248, s43, v252
	v_fma_f32 v232, v234, v232, v232
	v_fma_f32 v236, -v236, v227, v227
	v_add_u32_e32 v249, s43, v253
	v_rcp_f32_e32 v232, v232
	s_nop 0
	v_fma_f32 v231, -v231, v232, v232
	v_cvt_pk_f16_f32 v247, v236, v231
	ds_write_b64 v250, v[246:247] offset:8192
	v_mfma_f32_16x16x32_f16 v[210:213], v[66:69], v[154:157], v[210:213]
	v_mfma_f32_16x16x32_f16 v[214:217], v[78:81], v[154:157], v[214:217]
	v_mov_b32_e32 v245, v246
	v_mov_b32_e32 v187, v247
	buffer_load_dwordx2 v[192:193], v209, s[20:23], s45 offen
	s_add_i32 s40, s40, 1
	s_add_i32 s44, s44, 0x1000
	s_waitcnt lgkmcnt(0)
	s_barrier
	ds_read_b128 v[158:161], v248 offset:0
	ds_read_b128 v[162:165], v248 offset:1024
	ds_read_b128 v[166:169], v249 offset:2048
	ds_read_b128 v[170:173], v249 offset:3072
	v_mfma_f32_16x16x32_f16 v[218:221], v[82:85], v[150:153], v[106:109]
	v_mfma_f32_16x16x32_f16 v[222:225], v[90:93], v[150:153], v[110:113]
	v_mfma_f32_16x16x32_f16 v[218:221], v[86:89], v[154:157], v[218:221]
	v_mfma_f32_16x16x32_f16 v[222:225], v[94:97], v[154:157], v[222:225]
	s_waitcnt lgkmcnt(2)
	v_mfma_f32_16x16x32_f16 v[210:213], v[54:57], v[158:161], v[210:213]
	v_mfma_f32_16x16x32_f16 v[210:213], v[58:61], v[162:165], v[210:213]
	s_waitcnt lgkmcnt(0)
	v_mfma_f32_16x16x32_f16 v[210:213], v[62:65], v[166:169], v[210:213]
	v_mfma_f32_16x16x32_f16 v[210:213], v[50:53], v[170:173], v[210:213]
	s_waitcnt vmcnt(9)
	v_cvt_pk_f16_f32 v251, v190, v191
	ds_write_b32 v1, v251 offset:2048
	ds_read_b128 v[150:153], v186 offset:0
	ds_read_b128 v[154:157], v186 offset:1024
	s_add_i32 s45, s45, 0x100000
	s_add_i32 s46, s46, 0x4000
	s_movk_i32 s47, 0x1000
	s_add_i32 s43, s40, -12
	s_lshl_b32 s43, s43, 12
	s_cmp_lt_u32 s40, 14
	s_cselect_b32 s43, s47, s43
	v_exp_f32_e32 v226, v210
	v_exp_f32_e32 v227, v211
	v_mfma_f32_16x16x32_f16 v[214:217], v[34:37], v[158:161], v[214:217]
	v_min_f32_e32 v228, s42, v212
	v_exp_f32_e32 v229, v213
	v_mfma_f32_16x16x32_f16 v[214:217], v[38:41], v[162:165], v[214:217]
	v_exp_f32_e32 v228, v228
	v_add_f32_e32 v227, 1.0, v227
	v_mfma_f32_16x16x32_f16 v[214:217], v[42:45], v[166:169], v[214:217]
	v_fma_f32 v230, v228, s41, s41
	v_rcp_f32_e32 v227, v227
	v_mfma_f32_16x16x32_f16 v[214:217], v[46:49], v[170:173], v[214:217]
	v_fma_f32 v230, v226, v230, v230
	v_rcp_f32_e32 v230, v230
	v_mfma_f32_16x16x32_f16 v[218:221], v[18:21], v[158:161], v[218:221]
	v_fma_f32 v226, -v228, v230, v230
	v_fma_f32 v200, v200, v227, v226
	v_mfma_f32_16x16x32_f16 v[218:221], v[14:17], v[162:165], v[218:221]
	v_min_f32_e32 v226, s42, v200
	v_exp_f32_e32 v226, v226
	v_mfma_f32_16x16x32_f16 v[218:221], v[10:13], v[166:169], v[218:221]
	v_add_f32_e32 v227, 1.0, v226
	v_fma_f32 v227, v229, v227, v227
	v_mfma_f32_16x16x32_f16 v[218:221], v[26:29], v[170:173], v[218:221]
	v_rcp_f32_e32 v227, v227
	v_exp_f32_e32 v231, v214
	v_mfma_f32_16x16x32_f16 v[222:225], v[2:5], v[158:161], v[222:225]
	v_exp_f32_e32 v232, v215
	v_fma_f32 v226, -v226, v227, v227
	v_mfma_f32_16x16x32_f16 v[222:225], v[6:9], v[162:165], v[222:225]
	v_min_f32_e32 v233, s42, v216
	v_exp_f32_e32 v234, v217
	v_mfma_f32_16x16x32_f16 v[222:225], v[22:25], v[166:169], v[222:225]
	v_exp_f32_e32 v236, v218
	v_exp_f32_e32 v233, v233
	v_mfma_f32_16x16x32_f16 v[222:225], v[30:33], v[170:173], v[222:225]
	v_add_f32_e32 v232, 1.0, v232
	v_exp_f32_e32 v227, v219
	v_fma_f32 v235, v233, s41, s41
	v_rcp_f32_e32 v232, v232
	v_min_f32_e32 v228, s42, v220
	v_fma_f32 v235, v231, v235, v235
	v_rcp_f32_e32 v235, v235
	v_exp_f32_e32 v229, v221
	v_fma_f32 v231, -v233, v235, v235
	v_fma_f32 v201, v201, v232, v231
	v_exp_f32_e32 v228, v228
	v_min_f32_e32 v231, s42, v201
	v_exp_f32_e32 v231, v231
	v_add_f32_e32 v227, 1.0, v227
	v_add_f32_e32 v232, 1.0, v231
	v_mfma_f32_16x16x32_f16 v[146:149], v[114:117], v[158:161], v[146:149]
	v_fma_f32 v232, v234, v232, v232
	v_fma_f32 v230, v228, s41, s41
	v_rcp_f32_e32 v232, v232
	v_mfma_f32_16x16x32_f16 v[146:149], v[118:121], v[162:165], v[146:149]
	v_fma_f32 v231, -v231, v232, v232
	v_rcp_f32_e32 v227, v227
	v_cvt_pk_f16_f32 v246, v226, v231
	buffer_load_dwordx4 v[114:117], v189, s[16:19], s46 offen
	buffer_load_dwordx4 v[118:121], v208, s[16:19], s46 offen
	v_exp_f32_e32 v231, v222
	v_fma_f32 v230, v236, v230, v230
	v_exp_f32_e32 v232, v223
	s_waitcnt lgkmcnt(0)
	v_mfma_f32_16x16x32_f16 v[210:213], v[70:73], v[150:153], v[98:101]
	v_min_f32_e32 v233, s42, v224
	v_rcp_f32_e32 v230, v230
	v_exp_f32_e32 v234, v225
	v_mfma_f32_16x16x32_f16 v[214:217], v[74:77], v[150:153], v[102:105]
	v_exp_f32_e32 v233, v233
	v_fma_f32 v236, -v228, v230, v230
	v_add_f32_e32 v232, 1.0, v232
	v_fma_f32 v235, v233, s41, s41
	v_fma_f32 v198, v198, v227, v236
	v_rcp_f32_e32 v232, v232
	v_fma_f32 v235, v231, v235, v235
	v_min_f32_e32 v236, s42, v198
	v_rcp_f32_e32 v235, v235
	s_nop 0
	v_fma_f32 v231, -v233, v235, v235
	v_exp_f32_e32 v236, v236
	v_fma_f32 v199, v199, v232, v231
	v_min_f32_e32 v231, s42, v199
	v_add_f32_e32 v227, 1.0, v236
	v_exp_f32_e32 v231, v231
	v_fma_f32 v227, v229, v227, v227
	v_add_u32_e32 v250, s43, v206
	v_add_f32_e32 v232, 1.0, v231
	v_rcp_f32_e32 v227, v227
	v_add_u32_e32 v248, s43, v252
	v_fma_f32 v232, v234, v232, v232
	v_fma_f32 v236, -v236, v227, v227
	v_add_u32_e32 v249, s43, v253
	v_rcp_f32_e32 v232, v232
	s_nop 0
	v_fma_f32 v231, -v231, v232, v232
	v_cvt_pk_f16_f32 v247, v236, v231
	ds_write_b64 v250, v[246:247] offset:8192
	v_mfma_f32_16x16x32_f16 v[210:213], v[66:69], v[154:157], v[210:213]
	v_mfma_f32_16x16x32_f16 v[214:217], v[78:81], v[154:157], v[214:217]
	v_mov_b32_e32 v188, v246
	v_mov_b32_e32 v202, v247
	buffer_load_dwordx2 v[190:191], v209, s[20:23], s45 offen
	s_add_i32 s40, s40, 1
	s_add_i32 s44, s44, 0x1000
	s_waitcnt lgkmcnt(0)
	s_barrier
	ds_read_b128 v[158:161], v248 offset:0
	ds_read_b128 v[162:165], v248 offset:1024
	ds_read_b128 v[166:169], v249 offset:2048
	ds_read_b128 v[170:173], v249 offset:3072
	v_mfma_f32_16x16x32_f16 v[218:221], v[82:85], v[150:153], v[106:109]
	v_mfma_f32_16x16x32_f16 v[222:225], v[90:93], v[150:153], v[110:113]
	v_mfma_f32_16x16x32_f16 v[218:221], v[86:89], v[154:157], v[218:221]
	v_mfma_f32_16x16x32_f16 v[222:225], v[94:97], v[154:157], v[222:225]
	s_waitcnt lgkmcnt(2)
	v_mfma_f32_16x16x32_f16 v[210:213], v[54:57], v[158:161], v[210:213]
	v_mfma_f32_16x16x32_f16 v[210:213], v[58:61], v[162:165], v[210:213]
	s_waitcnt lgkmcnt(0)
	v_mfma_f32_16x16x32_f16 v[210:213], v[62:65], v[166:169], v[210:213]
	v_mfma_f32_16x16x32_f16 v[210:213], v[50:53], v[170:173], v[210:213]
	s_waitcnt vmcnt(9)
	v_cvt_pk_f16_f32 v251, v196, v197
	ds_write_b32 v1, v251 offset:4096
	ds_read_b128 v[150:153], v186 offset:2048
	ds_read_b128 v[154:157], v186 offset:3072
	s_add_i32 s45, s45, 0x100000
	s_add_i32 s46, s46, 0x4000
	s_movk_i32 s47, 0x0
	s_add_i32 s43, s40, -12
	s_lshl_b32 s43, s43, 12
	s_cmp_lt_u32 s40, 14
	s_cselect_b32 s43, s47, s43
	v_exp_f32_e32 v226, v210
	v_exp_f32_e32 v227, v211
	v_mfma_f32_16x16x32_f16 v[214:217], v[34:37], v[158:161], v[214:217]
	v_min_f32_e32 v228, s42, v212
	v_exp_f32_e32 v229, v213
	v_mfma_f32_16x16x32_f16 v[214:217], v[38:41], v[162:165], v[214:217]
	v_exp_f32_e32 v228, v228
	v_add_f32_e32 v227, 1.0, v227
	v_mfma_f32_16x16x32_f16 v[214:217], v[42:45], v[166:169], v[214:217]
	v_fma_f32 v230, v228, s41, s41
	v_rcp_f32_e32 v227, v227
	v_mfma_f32_16x16x32_f16 v[214:217], v[46:49], v[170:173], v[214:217]
	v_fma_f32 v230, v226, v230, v230
	v_rcp_f32_e32 v230, v230
	v_mfma_f32_16x16x32_f16 v[218:221], v[18:21], v[158:161], v[218:221]
	v_fma_f32 v226, -v228, v230, v230
	v_fma_f32 v200, v200, v227, v226
	v_mfma_f32_16x16x32_f16 v[218:221], v[14:17], v[162:165], v[218:221]
	v_min_f32_e32 v226, s42, v200
	v_exp_f32_e32 v226, v226
	v_mfma_f32_16x16x32_f16 v[218:221], v[10:13], v[166:169], v[218:221]
	v_add_f32_e32 v227, 1.0, v226
	v_fma_f32 v227, v229, v227, v227
	v_mfma_f32_16x16x32_f16 v[218:221], v[26:29], v[170:173], v[218:221]
	v_rcp_f32_e32 v227, v227
	v_exp_f32_e32 v231, v214
	v_mfma_f32_16x16x32_f16 v[222:225], v[2:5], v[158:161], v[222:225]
	v_exp_f32_e32 v232, v215
	v_fma_f32 v226, -v226, v227, v227
	v_mfma_f32_16x16x32_f16 v[222:225], v[6:9], v[162:165], v[222:225]
	v_min_f32_e32 v233, s42, v216
	v_exp_f32_e32 v234, v217
	v_mfma_f32_16x16x32_f16 v[222:225], v[22:25], v[166:169], v[222:225]
	v_exp_f32_e32 v236, v218
	v_exp_f32_e32 v233, v233
	v_mfma_f32_16x16x32_f16 v[222:225], v[30:33], v[170:173], v[222:225]
	v_add_f32_e32 v232, 1.0, v232
	v_exp_f32_e32 v227, v219
	v_fma_f32 v235, v233, s41, s41
	v_rcp_f32_e32 v232, v232
	v_min_f32_e32 v228, s42, v220
	v_fma_f32 v235, v231, v235, v235
	v_rcp_f32_e32 v235, v235
	v_exp_f32_e32 v229, v221
	v_fma_f32 v231, -v233, v235, v235
	v_fma_f32 v201, v201, v232, v231
	v_exp_f32_e32 v228, v228
	v_min_f32_e32 v231, s42, v201
	v_exp_f32_e32 v231, v231
	v_add_f32_e32 v227, 1.0, v227
	v_add_f32_e32 v232, 1.0, v231
	v_mfma_f32_16x16x32_f16 v[146:149], v[138:141], v[158:161], v[146:149]
	v_fma_f32 v232, v234, v232, v232
	v_fma_f32 v230, v228, s41, s41
	v_rcp_f32_e32 v232, v232
	v_mfma_f32_16x16x32_f16 v[146:149], v[142:145], v[162:165], v[146:149]
	v_fma_f32 v231, -v231, v232, v232
	v_rcp_f32_e32 v227, v227
	v_cvt_pk_f16_f32 v246, v226, v231
	buffer_load_dwordx4 v[138:141], v189, s[16:19], s46 offen
	buffer_load_dwordx4 v[142:145], v208, s[16:19], s46 offen
	v_exp_f32_e32 v231, v222
	v_fma_f32 v230, v236, v230, v230
	v_exp_f32_e32 v232, v223
	s_waitcnt lgkmcnt(0)
	v_mfma_f32_16x16x32_f16 v[210:213], v[70:73], v[150:153], v[98:101]
	v_min_f32_e32 v233, s42, v224
	v_rcp_f32_e32 v230, v230
	v_exp_f32_e32 v234, v225
	v_mfma_f32_16x16x32_f16 v[214:217], v[74:77], v[150:153], v[102:105]
	v_exp_f32_e32 v233, v233
	v_fma_f32 v236, -v228, v230, v230
	v_add_f32_e32 v232, 1.0, v232
	v_fma_f32 v235, v233, s41, s41
	v_fma_f32 v198, v198, v227, v236
	v_rcp_f32_e32 v232, v232
	v_fma_f32 v235, v231, v235, v235
	v_min_f32_e32 v236, s42, v198
	v_rcp_f32_e32 v235, v235
	s_nop 0
	v_fma_f32 v231, -v233, v235, v235
	v_exp_f32_e32 v236, v236
	v_fma_f32 v199, v199, v232, v231
	v_min_f32_e32 v231, s42, v199
	v_add_f32_e32 v227, 1.0, v236
	v_exp_f32_e32 v231, v231
	v_fma_f32 v227, v229, v227, v227
	v_add_u32_e32 v250, s43, v206
	v_add_f32_e32 v232, 1.0, v231
	v_rcp_f32_e32 v227, v227
	v_add_u32_e32 v248, s43, v252
	v_fma_f32 v232, v234, v232, v232
	v_fma_f32 v236, -v236, v227, v227
	v_add_u32_e32 v249, s43, v253
	v_rcp_f32_e32 v232, v232
	s_nop 0
	v_fma_f32 v231, -v231, v232, v232
	v_cvt_pk_f16_f32 v247, v236, v231
	ds_write_b64 v250, v[246:247] offset:8192
	v_mfma_f32_16x16x32_f16 v[210:213], v[66:69], v[154:157], v[210:213]
	v_mfma_f32_16x16x32_f16 v[214:217], v[78:81], v[154:157], v[214:217]
	v_mov_b32_e32 v203, v246
	v_mov_b32_e32 v204, v247
	buffer_load_dwordx2 v[196:197], v209, s[20:23], s45 offen
	s_add_i32 s40, s40, 1
	s_add_i32 s44, s44, 0x1000
	s_waitcnt lgkmcnt(0)
	s_barrier
	ds_read_b128 v[158:161], v248 offset:0
	ds_read_b128 v[162:165], v248 offset:1024
	ds_read_b128 v[166:169], v249 offset:2048
	ds_read_b128 v[170:173], v249 offset:3072
	v_mfma_f32_16x16x32_f16 v[218:221], v[82:85], v[150:153], v[106:109]
	v_mfma_f32_16x16x32_f16 v[222:225], v[90:93], v[150:153], v[110:113]
	v_mfma_f32_16x16x32_f16 v[218:221], v[86:89], v[154:157], v[218:221]
	v_mfma_f32_16x16x32_f16 v[222:225], v[94:97], v[154:157], v[222:225]
	s_waitcnt lgkmcnt(2)
	v_mfma_f32_16x16x32_f16 v[210:213], v[54:57], v[158:161], v[210:213]
	v_mfma_f32_16x16x32_f16 v[210:213], v[58:61], v[162:165], v[210:213]
	s_waitcnt lgkmcnt(0)
	v_mfma_f32_16x16x32_f16 v[210:213], v[62:65], v[166:169], v[210:213]
	v_mfma_f32_16x16x32_f16 v[210:213], v[50:53], v[170:173], v[210:213]
	s_waitcnt vmcnt(9)
	v_cvt_pk_f16_f32 v251, v194, v195
	ds_write_b32 v1, v251 offset:6144
	ds_read_b128 v[150:153], v186 offset:4096
	ds_read_b128 v[154:157], v186 offset:5120
	s_add_i32 s45, s45, 0x100000
	s_add_i32 s46, s46, 0x4000
	s_movk_i32 s47, 0x1000
	s_add_i32 s43, s40, -12
	s_lshl_b32 s43, s43, 12
	s_cmp_lt_u32 s40, 14
	s_cselect_b32 s43, s47, s43
	v_exp_f32_e32 v226, v210
	v_exp_f32_e32 v227, v211
	v_mfma_f32_16x16x32_f16 v[214:217], v[34:37], v[158:161], v[214:217]
	v_min_f32_e32 v228, s42, v212
	v_exp_f32_e32 v229, v213
	v_mfma_f32_16x16x32_f16 v[214:217], v[38:41], v[162:165], v[214:217]
	v_exp_f32_e32 v228, v228
	v_add_f32_e32 v227, 1.0, v227
	v_mfma_f32_16x16x32_f16 v[214:217], v[42:45], v[166:169], v[214:217]
	v_fma_f32 v230, v228, s41, s41
	v_rcp_f32_e32 v227, v227
	v_mfma_f32_16x16x32_f16 v[214:217], v[46:49], v[170:173], v[214:217]
	v_fma_f32 v230, v226, v230, v230
	v_rcp_f32_e32 v230, v230
	v_mfma_f32_16x16x32_f16 v[218:221], v[18:21], v[158:161], v[218:221]
	v_fma_f32 v226, -v228, v230, v230
	v_fma_f32 v200, v200, v227, v226
	v_mfma_f32_16x16x32_f16 v[218:221], v[14:17], v[162:165], v[218:221]
	v_min_f32_e32 v226, s42, v200
	v_exp_f32_e32 v226, v226
	v_mfma_f32_16x16x32_f16 v[218:221], v[10:13], v[166:169], v[218:221]
	v_add_f32_e32 v227, 1.0, v226
	v_fma_f32 v227, v229, v227, v227
	v_mfma_f32_16x16x32_f16 v[218:221], v[26:29], v[170:173], v[218:221]
	v_rcp_f32_e32 v227, v227
	v_exp_f32_e32 v231, v214
	v_mfma_f32_16x16x32_f16 v[222:225], v[2:5], v[158:161], v[222:225]
	v_exp_f32_e32 v232, v215
	v_fma_f32 v226, -v226, v227, v227
	v_mfma_f32_16x16x32_f16 v[222:225], v[6:9], v[162:165], v[222:225]
	v_min_f32_e32 v233, s42, v216
	v_exp_f32_e32 v234, v217
	v_mfma_f32_16x16x32_f16 v[222:225], v[22:25], v[166:169], v[222:225]
	v_exp_f32_e32 v236, v218
	v_exp_f32_e32 v233, v233
	v_mfma_f32_16x16x32_f16 v[222:225], v[30:33], v[170:173], v[222:225]
	v_add_f32_e32 v232, 1.0, v232
	v_exp_f32_e32 v227, v219
	v_fma_f32 v235, v233, s41, s41
	v_rcp_f32_e32 v232, v232
	v_min_f32_e32 v228, s42, v220
	v_fma_f32 v235, v231, v235, v235
	v_rcp_f32_e32 v235, v235
	v_exp_f32_e32 v229, v221
	v_fma_f32 v231, -v233, v235, v235
	v_fma_f32 v201, v201, v232, v231
	v_exp_f32_e32 v228, v228
	v_min_f32_e32 v231, s42, v201
	v_exp_f32_e32 v231, v231
	v_add_f32_e32 v227, 1.0, v227
	v_add_f32_e32 v232, 1.0, v231
	v_mfma_f32_16x16x32_f16 v[146:149], v[130:133], v[158:161], v[146:149]
	v_fma_f32 v232, v234, v232, v232
	v_fma_f32 v230, v228, s41, s41
	v_rcp_f32_e32 v232, v232
	v_mfma_f32_16x16x32_f16 v[146:149], v[134:137], v[162:165], v[146:149]
	v_fma_f32 v231, -v231, v232, v232
	v_rcp_f32_e32 v227, v227
	v_cvt_pk_f16_f32 v246, v226, v231
	buffer_load_dwordx4 v[130:133], v189, s[16:19], s46 offen
	buffer_load_dwordx4 v[134:137], v208, s[16:19], s46 offen
	v_exp_f32_e32 v231, v222
	v_fma_f32 v230, v236, v230, v230
	v_exp_f32_e32 v232, v223
	s_waitcnt lgkmcnt(0)
	v_mfma_f32_16x16x32_f16 v[210:213], v[70:73], v[150:153], v[98:101]
	v_min_f32_e32 v233, s42, v224
	v_rcp_f32_e32 v230, v230
	v_exp_f32_e32 v234, v225
	v_mfma_f32_16x16x32_f16 v[214:217], v[74:77], v[150:153], v[102:105]
	v_exp_f32_e32 v233, v233
	v_fma_f32 v236, -v228, v230, v230
	v_add_f32_e32 v232, 1.0, v232
	v_fma_f32 v235, v233, s41, s41
	v_fma_f32 v198, v198, v227, v236
	v_rcp_f32_e32 v232, v232
	v_fma_f32 v235, v231, v235, v235
	v_min_f32_e32 v236, s42, v198
	v_rcp_f32_e32 v235, v235
	s_nop 0
	v_fma_f32 v231, -v233, v235, v235
	v_exp_f32_e32 v236, v236
	v_fma_f32 v199, v199, v232, v231
	v_min_f32_e32 v231, s42, v199
	v_add_f32_e32 v227, 1.0, v236
	v_exp_f32_e32 v231, v231
	v_fma_f32 v227, v229, v227, v227
	v_add_u32_e32 v250, s43, v206
	v_add_f32_e32 v232, 1.0, v231
	v_rcp_f32_e32 v227, v227
	v_add_u32_e32 v248, s43, v252
	v_fma_f32 v232, v234, v232, v232
	v_fma_f32 v236, -v236, v227, v227
	v_add_u32_e32 v249, s43, v253
	v_rcp_f32_e32 v232, v232
	s_nop 0
	v_fma_f32 v231, -v231, v232, v232
	v_cvt_pk_f16_f32 v247, v236, v231
	ds_write_b64 v250, v[246:247] offset:8192
	v_mfma_f32_16x16x32_f16 v[210:213], v[66:69], v[154:157], v[210:213]
	v_mfma_f32_16x16x32_f16 v[214:217], v[78:81], v[154:157], v[214:217]
	v_mov_b32_e32 v205, v246
	v_mov_b32_e32 v207, v247
	buffer_load_dwordx2 v[194:195], v209, s[20:23], s45 offen
	s_add_i32 s40, s40, 1
	s_add_i32 s44, s44, 0x1000
	s_waitcnt lgkmcnt(0)
	s_barrier
	s_mov_b32 s45, 0xc00000
	s_mov_b32 s46, 0x30000
.Lmy_loopb:
	ds_read_b128 v[158:161], v248 offset:0
	ds_read_b128 v[162:165], v248 offset:1024
	ds_read_b128 v[166:169], v249 offset:2048
	ds_read_b128 v[170:173], v249 offset:3072
	v_mfma_f32_16x16x32_f16 v[218:221], v[82:85], v[150:153], v[106:109]
	v_mfma_f32_16x16x32_f16 v[222:225], v[90:93], v[150:153], v[110:113]
	v_mfma_f32_16x16x32_f16 v[218:221], v[86:89], v[154:157], v[218:221]
	v_mfma_f32_16x16x32_f16 v[222:225], v[94:97], v[154:157], v[222:225]
	s_waitcnt lgkmcnt(2)
	v_mfma_f32_16x16x32_f16 v[210:213], v[54:57], v[158:161], v[210:213]
	v_mfma_f32_16x16x32_f16 v[210:213], v[58:61], v[162:165], v[210:213]
	s_waitcnt lgkmcnt(0)
	v_mfma_f32_16x16x32_f16 v[210:213], v[62:65], v[166:169], v[210:213]
	v_mfma_f32_16x16x32_f16 v[210:213], v[50:53], v[170:173], v[210:213]
	s_waitcnt vmcnt(9)
	v_cvt_pk_f16_f32 v251, v192, v193
	ds_write_b32 v1, v251 offset:0
	ds_read_b128 v[150:153], v186 offset:6144
	ds_read_b128 v[154:157], v186 offset:7168
	v_add_u32_e32 v250, 0x1000, v250
	v_add_u32_e32 v248, 0x1000, v248
	v_add_u32_e32 v249, 0x1000, v249
	v_exp_f32_e32 v226, v210
	v_exp_f32_e32 v227, v211
	v_mfma_f32_16x16x32_f16 v[214:217], v[34:37], v[158:161], v[214:217]
	v_min_f32_e32 v228, s42, v212
	v_exp_f32_e32 v229, v213
	v_mfma_f32_16x16x32_f16 v[214:217], v[38:41], v[162:165], v[214:217]
	v_exp_f32_e32 v228, v228
	v_add_f32_e32 v227, 1.0, v227
	v_mfma_f32_16x16x32_f16 v[214:217], v[42:45], v[166:169], v[214:217]
	v_fma_f32 v230, v228, s41, s41
	v_rcp_f32_e32 v227, v227
	v_mfma_f32_16x16x32_f16 v[214:217], v[46:49], v[170:173], v[214:217]
	v_fma_f32 v230, v226, v230, v230
	v_rcp_f32_e32 v230, v230
	v_mfma_f32_16x16x32_f16 v[218:221], v[18:21], v[158:161], v[218:221]
	v_fma_f32 v226, -v228, v230, v230
	v_fma_f32 v200, v200, v227, v226
	v_mfma_f32_16x16x32_f16 v[218:221], v[14:17], v[162:165], v[218:221]
	v_min_f32_e32 v226, s42, v200
	v_exp_f32_e32 v226, v226
	v_mfma_f32_16x16x32_f16 v[218:221], v[10:13], v[166:169], v[218:221]
	v_add_f32_e32 v227, 1.0, v226
	v_fma_f32 v227, v229, v227, v227
	v_mfma_f32_16x16x32_f16 v[218:221], v[26:29], v[170:173], v[218:221]
	v_rcp_f32_e32 v227, v227
	v_exp_f32_e32 v231, v214
	v_mfma_f32_16x16x32_f16 v[222:225], v[2:5], v[158:161], v[222:225]
	v_exp_f32_e32 v232, v215
	v_fma_f32 v226, -v226, v227, v227
	v_mfma_f32_16x16x32_f16 v[222:225], v[6:9], v[162:165], v[222:225]
	v_min_f32_e32 v233, s42, v216
	v_exp_f32_e32 v234, v217
	v_mfma_f32_16x16x32_f16 v[222:225], v[22:25], v[166:169], v[222:225]
	v_exp_f32_e32 v236, v218
	v_exp_f32_e32 v233, v233
	v_mfma_f32_16x16x32_f16 v[222:225], v[30:33], v[170:173], v[222:225]
	v_add_f32_e32 v232, 1.0, v232
	v_exp_f32_e32 v227, v219
	v_fma_f32 v235, v233, s41, s41
	v_rcp_f32_e32 v232, v232
	v_min_f32_e32 v228, s42, v220
	v_fma_f32 v235, v231, v235, v235
	v_rcp_f32_e32 v235, v235
	v_exp_f32_e32 v229, v221
	v_fma_f32 v231, -v233, v235, v235
	v_fma_f32 v201, v201, v232, v231
	v_exp_f32_e32 v228, v228
	v_min_f32_e32 v231, s42, v201
	v_exp_f32_e32 v231, v231
	v_add_f32_e32 v227, 1.0, v227
	v_add_f32_e32 v232, 1.0, v231
	v_mfma_f32_16x16x32_f16 v[146:149], v[122:125], v[158:161], v[146:149]
	v_fma_f32 v232, v234, v232, v232
	v_fma_f32 v230, v228, s41, s41
	v_rcp_f32_e32 v232, v232
	v_mfma_f32_16x16x32_f16 v[146:149], v[126:129], v[162:165], v[146:149]
	v_fma_f32 v231, -v231, v232, v232
	v_rcp_f32_e32 v227, v227
	v_cvt_pk_f16_f32 v246, v226, v231
	buffer_load_dwordx4 v[122:125], v189, s[76:79], s46 offen
	buffer_load_dwordx4 v[126:129], v208, s[76:79], s46 offen
	v_exp_f32_e32 v231, v222
	v_fma_f32 v230, v236, v230, v230
	v_exp_f32_e32 v232, v223
	s_waitcnt lgkmcnt(0)
	v_mfma_f32_16x16x32_f16 v[210:213], v[70:73], v[150:153], v[98:101]
	v_min_f32_e32 v233, s42, v224
	v_rcp_f32_e32 v230, v230
	v_exp_f32_e32 v234, v225
	v_mfma_f32_16x16x32_f16 v[214:217], v[74:77], v[150:153], v[102:105]
	v_exp_f32_e32 v233, v233
	v_fma_f32 v236, -v228, v230, v230
	v_add_f32_e32 v232, 1.0, v232
	v_fma_f32 v235, v233, s41, s41
	v_fma_f32 v198, v198, v227, v236
	v_rcp_f32_e32 v232, v232
	v_fma_f32 v235, v231, v235, v235
	v_min_f32_e32 v236, s42, v198
	v_rcp_f32_e32 v235, v235
	s_nop 0
	v_fma_f32 v231, -v233, v235, v235
	v_exp_f32_e32 v236, v236
	v_fma_f32 v199, v199, v232, v231
	v_min_f32_e32 v231, s42, v199
	v_add_f32_e32 v227, 1.0, v236
	v_exp_f32_e32 v231, v231
	v_fma_f32 v227, v229, v227, v227
	v_add_f32_e32 v232, 1.0, v231
	v_rcp_f32_e32 v227, v227
	v_fma_f32 v232, v234, v232, v232
	v_fma_f32 v236, -v236, v227, v227
	v_rcp_f32_e32 v232, v232
	s_nop 0
	v_fma_f32 v231, -v231, v232, v232
	v_cvt_pk_f16_f32 v247, v236, v231
	ds_write_b64 v250, v[246:247] offset:8192
	v_mfma_f32_16x16x32_f16 v[210:213], v[66:69], v[154:157], v[210:213]
	v_mfma_f32_16x16x32_f16 v[214:217], v[78:81], v[154:157], v[214:217]
	buffer_load_dwordx2 v[192:193], v209, s[56:59], s45 offen
	s_waitcnt lgkmcnt(0)
	s_barrier
	ds_read_b128 v[158:161], v248 offset:0
	ds_read_b128 v[162:165], v248 offset:1024
	ds_read_b128 v[166:169], v249 offset:2048
	ds_read_b128 v[170:173], v249 offset:3072
	v_mfma_f32_16x16x32_f16 v[218:221], v[82:85], v[150:153], v[106:109]
	v_mfma_f32_16x16x32_f16 v[222:225], v[90:93], v[150:153], v[110:113]
	v_mfma_f32_16x16x32_f16 v[218:221], v[86:89], v[154:157], v[218:221]
	v_mfma_f32_16x16x32_f16 v[222:225], v[94:97], v[154:157], v[222:225]
	s_waitcnt lgkmcnt(2)
	v_mfma_f32_16x16x32_f16 v[210:213], v[54:57], v[158:161], v[210:213]
	v_mfma_f32_16x16x32_f16 v[210:213], v[58:61], v[162:165], v[210:213]
	s_waitcnt lgkmcnt(0)
	v_mfma_f32_16x16x32_f16 v[210:213], v[62:65], v[166:169], v[210:213]
	v_mfma_f32_16x16x32_f16 v[210:213], v[50:53], v[170:173], v[210:213]
	s_waitcnt vmcnt(9)
	v_cvt_pk_f16_f32 v251, v190, v191
	ds_write_b32 v1, v251 offset:2048
	ds_read_b128 v[150:153], v186 offset:0
	ds_read_b128 v[154:157], v186 offset:1024
	v_add_u32_e32 v250, 0x1000, v250
	v_add_u32_e32 v248, 0x1000, v248
	v_add_u32_e32 v249, 0x1000, v249
	v_exp_f32_e32 v226, v210
	v_exp_f32_e32 v227, v211
	v_mfma_f32_16x16x32_f16 v[214:217], v[34:37], v[158:161], v[214:217]
	v_min_f32_e32 v228, s42, v212
	v_exp_f32_e32 v229, v213
	v_mfma_f32_16x16x32_f16 v[214:217], v[38:41], v[162:165], v[214:217]
	v_exp_f32_e32 v228, v228
	v_add_f32_e32 v227, 1.0, v227
	v_mfma_f32_16x16x32_f16 v[214:217], v[42:45], v[166:169], v[214:217]
	v_fma_f32 v230, v228, s41, s41
	v_rcp_f32_e32 v227, v227
	v_mfma_f32_16x16x32_f16 v[214:217], v[46:49], v[170:173], v[214:217]
	v_fma_f32 v230, v226, v230, v230
	v_rcp_f32_e32 v230, v230
	v_mfma_f32_16x16x32_f16 v[218:221], v[18:21], v[158:161], v[218:221]
	v_fma_f32 v226, -v228, v230, v230
	v_fma_f32 v200, v200, v227, v226
	v_mfma_f32_16x16x32_f16 v[218:221], v[14:17], v[162:165], v[218:221]
	v_min_f32_e32 v226, s42, v200
	v_exp_f32_e32 v226, v226
	v_mfma_f32_16x16x32_f16 v[218:221], v[10:13], v[166:169], v[218:221]
	v_add_f32_e32 v227, 1.0, v226
	v_fma_f32 v227, v229, v227, v227
	v_mfma_f32_16x16x32_f16 v[218:221], v[26:29], v[170:173], v[218:221]
	v_rcp_f32_e32 v227, v227
	v_exp_f32_e32 v231, v214
	v_mfma_f32_16x16x32_f16 v[222:225], v[2:5], v[158:161], v[222:225]
	v_exp_f32_e32 v232, v215
	v_fma_f32 v226, -v226, v227, v227
	v_mfma_f32_16x16x32_f16 v[222:225], v[6:9], v[162:165], v[222:225]
	v_min_f32_e32 v233, s42, v216
	v_exp_f32_e32 v234, v217
	v_mfma_f32_16x16x32_f16 v[222:225], v[22:25], v[166:169], v[222:225]
	v_exp_f32_e32 v236, v218
	v_exp_f32_e32 v233, v233
	v_mfma_f32_16x16x32_f16 v[222:225], v[30:33], v[170:173], v[222:225]
	v_add_f32_e32 v232, 1.0, v232
	v_exp_f32_e32 v227, v219
	v_fma_f32 v235, v233, s41, s41
	v_rcp_f32_e32 v232, v232
	v_min_f32_e32 v228, s42, v220
	v_fma_f32 v235, v231, v235, v235
	v_rcp_f32_e32 v235, v235
	v_exp_f32_e32 v229, v221
	v_fma_f32 v231, -v233, v235, v235
	v_fma_f32 v201, v201, v232, v231
	v_exp_f32_e32 v228, v228
	v_min_f32_e32 v231, s42, v201
	v_exp_f32_e32 v231, v231
	v_add_f32_e32 v227, 1.0, v227
	v_add_f32_e32 v232, 1.0, v231
	v_mfma_f32_16x16x32_f16 v[146:149], v[114:117], v[158:161], v[146:149]
	v_fma_f32 v232, v234, v232, v232
	v_fma_f32 v230, v228, s41, s41
	v_rcp_f32_e32 v232, v232
	v_mfma_f32_16x16x32_f16 v[146:149], v[118:121], v[162:165], v[146:149]
	v_fma_f32 v231, -v231, v232, v232
	v_rcp_f32_e32 v227, v227
	v_cvt_pk_f16_f32 v246, v226, v231
	buffer_load_dwordx4 v[114:117], v189, s[80:83], s46 offen
	buffer_load_dwordx4 v[118:121], v208, s[80:83], s46 offen
	v_exp_f32_e32 v231, v222
	v_fma_f32 v230, v236, v230, v230
	v_exp_f32_e32 v232, v223
	s_waitcnt lgkmcnt(0)
	v_mfma_f32_16x16x32_f16 v[210:213], v[70:73], v[150:153], v[98:101]
	v_min_f32_e32 v233, s42, v224
	v_rcp_f32_e32 v230, v230
	v_exp_f32_e32 v234, v225
	v_mfma_f32_16x16x32_f16 v[214:217], v[74:77], v[150:153], v[102:105]
	v_exp_f32_e32 v233, v233
	v_fma_f32 v236, -v228, v230, v230
	v_add_f32_e32 v232, 1.0, v232
	v_fma_f32 v235, v233, s41, s41
	v_fma_f32 v198, v198, v227, v236
	v_rcp_f32_e32 v232, v232
	v_fma_f32 v235, v231, v235, v235
	v_min_f32_e32 v236, s42, v198
	v_rcp_f32_e32 v235, v235
	s_nop 0
	v_fma_f32 v231, -v233, v235, v235
	v_exp_f32_e32 v236, v236
	v_fma_f32 v199, v199, v232, v231
	v_min_f32_e32 v231, s42, v199
	v_add_f32_e32 v227, 1.0, v236
	v_exp_f32_e32 v231, v231
	v_fma_f32 v227, v229, v227, v227
	v_add_f32_e32 v232, 1.0, v231
	v_rcp_f32_e32 v227, v227
	v_fma_f32 v232, v234, v232, v232
	v_fma_f32 v236, -v236, v227, v227
	v_rcp_f32_e32 v232, v232
	s_nop 0
	v_fma_f32 v231, -v231, v232, v232
	v_cvt_pk_f16_f32 v247, v236, v231
	ds_write_b64 v250, v[246:247] offset:8192
	v_mfma_f32_16x16x32_f16 v[210:213], v[66:69], v[154:157], v[210:213]
	v_mfma_f32_16x16x32_f16 v[214:217], v[78:81], v[154:157], v[214:217]
	buffer_load_dwordx2 v[190:191], v209, s[60:63], s45 offen
	s_add_i32 s45, s45, 0x400000
	s_add_i32 s46, s46, 0x10000
	s_waitcnt lgkmcnt(0)
	s_barrier
	ds_read_b128 v[158:161], v248 offset:0
	ds_read_b128 v[162:165], v248 offset:1024
	ds_read_b128 v[166:169], v249 offset:2048
	ds_read_b128 v[170:173], v249 offset:3072
	v_mfma_f32_16x16x32_f16 v[218:221], v[82:85], v[150:153], v[106:109]
	v_mfma_f32_16x16x32_f16 v[222:225], v[90:93], v[150:153], v[110:113]
	v_mfma_f32_16x16x32_f16 v[218:221], v[86:89], v[154:157], v[218:221]
	v_mfma_f32_16x16x32_f16 v[222:225], v[94:97], v[154:157], v[222:225]
	s_waitcnt lgkmcnt(2)
	v_mfma_f32_16x16x32_f16 v[210:213], v[54:57], v[158:161], v[210:213]
	v_mfma_f32_16x16x32_f16 v[210:213], v[58:61], v[162:165], v[210:213]
	s_waitcnt lgkmcnt(0)
	v_mfma_f32_16x16x32_f16 v[210:213], v[62:65], v[166:169], v[210:213]
	v_mfma_f32_16x16x32_f16 v[210:213], v[50:53], v[170:173], v[210:213]
	s_waitcnt vmcnt(9)
	v_cvt_pk_f16_f32 v251, v196, v197
	ds_write_b32 v1, v251 offset:4096
	ds_read_b128 v[150:153], v186 offset:2048
	ds_read_b128 v[154:157], v186 offset:3072
	v_add_u32_e32 v250, 0x1000, v250
	v_add_u32_e32 v248, 0x1000, v248
	v_add_u32_e32 v249, 0x1000, v249
	v_exp_f32_e32 v226, v210
	v_exp_f32_e32 v227, v211
	v_mfma_f32_16x16x32_f16 v[214:217], v[34:37], v[158:161], v[214:217]
	v_min_f32_e32 v228, s42, v212
	v_exp_f32_e32 v229, v213
	v_mfma_f32_16x16x32_f16 v[214:217], v[38:41], v[162:165], v[214:217]
	v_exp_f32_e32 v228, v228
	v_add_f32_e32 v227, 1.0, v227
	v_mfma_f32_16x16x32_f16 v[214:217], v[42:45], v[166:169], v[214:217]
	v_fma_f32 v230, v228, s41, s41
	v_rcp_f32_e32 v227, v227
	v_mfma_f32_16x16x32_f16 v[214:217], v[46:49], v[170:173], v[214:217]
	v_fma_f32 v230, v226, v230, v230
	v_rcp_f32_e32 v230, v230
	v_mfma_f32_16x16x32_f16 v[218:221], v[18:21], v[158:161], v[218:221]
	v_fma_f32 v226, -v228, v230, v230
	v_fma_f32 v200, v200, v227, v226
	v_mfma_f32_16x16x32_f16 v[218:221], v[14:17], v[162:165], v[218:221]
	v_min_f32_e32 v226, s42, v200
	v_exp_f32_e32 v226, v226
	v_mfma_f32_16x16x32_f16 v[218:221], v[10:13], v[166:169], v[218:221]
	v_add_f32_e32 v227, 1.0, v226
	v_fma_f32 v227, v229, v227, v227
	v_mfma_f32_16x16x32_f16 v[218:221], v[26:29], v[170:173], v[218:221]
	v_rcp_f32_e32 v227, v227
	v_exp_f32_e32 v231, v214
	v_mfma_f32_16x16x32_f16 v[222:225], v[2:5], v[158:161], v[222:225]
	v_exp_f32_e32 v232, v215
	v_fma_f32 v226, -v226, v227, v227
	v_mfma_f32_16x16x32_f16 v[222:225], v[6:9], v[162:165], v[222:225]
	v_min_f32_e32 v233, s42, v216
	v_exp_f32_e32 v234, v217
	v_mfma_f32_16x16x32_f16 v[222:225], v[22:25], v[166:169], v[222:225]
	v_exp_f32_e32 v236, v218
	v_exp_f32_e32 v233, v233
	v_mfma_f32_16x16x32_f16 v[222:225], v[30:33], v[170:173], v[222:225]
	v_add_f32_e32 v232, 1.0, v232
	v_exp_f32_e32 v227, v219
	v_fma_f32 v235, v233, s41, s41
	v_rcp_f32_e32 v232, v232
	v_min_f32_e32 v228, s42, v220
	v_fma_f32 v235, v231, v235, v235
	v_rcp_f32_e32 v235, v235
	v_exp_f32_e32 v229, v221
	v_fma_f32 v231, -v233, v235, v235
	v_fma_f32 v201, v201, v232, v231
	v_exp_f32_e32 v228, v228
	v_min_f32_e32 v231, s42, v201
	v_exp_f32_e32 v231, v231
	v_add_f32_e32 v227, 1.0, v227
	v_add_f32_e32 v232, 1.0, v231
	v_mfma_f32_16x16x32_f16 v[146:149], v[138:141], v[158:161], v[146:149]
	v_fma_f32 v232, v234, v232, v232
	v_fma_f32 v230, v228, s41, s41
	v_rcp_f32_e32 v232, v232
	v_mfma_f32_16x16x32_f16 v[146:149], v[142:145], v[162:165], v[146:149]
	v_fma_f32 v231, -v231, v232, v232
	v_rcp_f32_e32 v227, v227
	v_cvt_pk_f16_f32 v246, v226, v231
	buffer_load_dwordx4 v[138:141], v189, s[68:71], s46 offen
	buffer_load_dwordx4 v[142:145], v208, s[68:71], s46 offen
	v_exp_f32_e32 v231, v222
	v_fma_f32 v230, v236, v230, v230
	v_exp_f32_e32 v232, v223
	s_waitcnt lgkmcnt(0)
	v_mfma_f32_16x16x32_f16 v[210:213], v[70:73], v[150:153], v[98:101]
	v_min_f32_e32 v233, s42, v224
	v_rcp_f32_e32 v230, v230
	v_exp_f32_e32 v234, v225
	v_mfma_f32_16x16x32_f16 v[214:217], v[74:77], v[150:153], v[102:105]
	v_exp_f32_e32 v233, v233
	v_fma_f32 v236, -v228, v230, v230
	v_add_f32_e32 v232, 1.0, v232
	v_fma_f32 v235, v233, s41, s41
	v_fma_f32 v198, v198, v227, v236
	v_rcp_f32_e32 v232, v232
	v_fma_f32 v235, v231, v235, v235
	v_min_f32_e32 v236, s42, v198
	v_rcp_f32_e32 v235, v235
	s_nop 0
	v_fma_f32 v231, -v233, v235, v235
	v_exp_f32_e32 v236, v236
	v_fma_f32 v199, v199, v232, v231
	v_min_f32_e32 v231, s42, v199
	v_add_f32_e32 v227, 1.0, v236
	v_exp_f32_e32 v231, v231
	v_fma_f32 v227, v229, v227, v227
	v_add_f32_e32 v232, 1.0, v231
	v_rcp_f32_e32 v227, v227
	v_fma_f32 v232, v234, v232, v232
	v_fma_f32 v236, -v236, v227, v227
	v_rcp_f32_e32 v232, v232
	s_nop 0
	v_fma_f32 v231, -v231, v232, v232
	v_cvt_pk_f16_f32 v247, v236, v231
	ds_write_b64 v250, v[246:247] offset:8192
	v_mfma_f32_16x16x32_f16 v[210:213], v[66:69], v[154:157], v[210:213]
	v_mfma_f32_16x16x32_f16 v[214:217], v[78:81], v[154:157], v[214:217]
	buffer_load_dwordx2 v[196:197], v209, s[48:51], s45 offen
	s_waitcnt lgkmcnt(0)
	s_barrier
	ds_read_b128 v[158:161], v248 offset:0
	ds_read_b128 v[162:165], v248 offset:1024
	ds_read_b128 v[166:169], v249 offset:2048
	ds_read_b128 v[170:173], v249 offset:3072
	v_mfma_f32_16x16x32_f16 v[218:221], v[82:85], v[150:153], v[106:109]
	v_mfma_f32_16x16x32_f16 v[222:225], v[90:93], v[150:153], v[110:113]
	v_mfma_f32_16x16x32_f16 v[218:221], v[86:89], v[154:157], v[218:221]
	v_mfma_f32_16x16x32_f16 v[222:225], v[94:97], v[154:157], v[222:225]
	s_waitcnt lgkmcnt(2)
	v_mfma_f32_16x16x32_f16 v[210:213], v[54:57], v[158:161], v[210:213]
	v_mfma_f32_16x16x32_f16 v[210:213], v[58:61], v[162:165], v[210:213]
	s_waitcnt lgkmcnt(0)
	v_mfma_f32_16x16x32_f16 v[210:213], v[62:65], v[166:169], v[210:213]
	v_mfma_f32_16x16x32_f16 v[210:213], v[50:53], v[170:173], v[210:213]
	s_waitcnt vmcnt(9)
	v_cvt_pk_f16_f32 v251, v194, v195
	ds_write_b32 v1, v251 offset:6144
	ds_read_b128 v[150:153], v186 offset:4096
	ds_read_b128 v[154:157], v186 offset:5120
	v_add_u32_e32 v250, 0x1000, v250
	v_add_u32_e32 v248, 0x1000, v248
	v_add_u32_e32 v249, 0x1000, v249
	v_exp_f32_e32 v226, v210
	v_exp_f32_e32 v227, v211
	v_mfma_f32_16x16x32_f16 v[214:217], v[34:37], v[158:161], v[214:217]
	v_min_f32_e32 v228, s42, v212
	v_exp_f32_e32 v229, v213
	v_mfma_f32_16x16x32_f16 v[214:217], v[38:41], v[162:165], v[214:217]
	v_exp_f32_e32 v228, v228
	v_add_f32_e32 v227, 1.0, v227
	v_mfma_f32_16x16x32_f16 v[214:217], v[42:45], v[166:169], v[214:217]
	v_fma_f32 v230, v228, s41, s41
	v_rcp_f32_e32 v227, v227
	v_mfma_f32_16x16x32_f16 v[214:217], v[46:49], v[170:173], v[214:217]
	v_fma_f32 v230, v226, v230, v230
	v_rcp_f32_e32 v230, v230
	v_mfma_f32_16x16x32_f16 v[218:221], v[18:21], v[158:161], v[218:221]
	v_fma_f32 v226, -v228, v230, v230
	v_fma_f32 v200, v200, v227, v226
	v_mfma_f32_16x16x32_f16 v[218:221], v[14:17], v[162:165], v[218:221]
	v_min_f32_e32 v226, s42, v200
	v_exp_f32_e32 v226, v226
	v_mfma_f32_16x16x32_f16 v[218:221], v[10:13], v[166:169], v[218:221]
	v_add_f32_e32 v227, 1.0, v226
	v_fma_f32 v227, v229, v227, v227
	v_mfma_f32_16x16x32_f16 v[218:221], v[26:29], v[170:173], v[218:221]
	v_rcp_f32_e32 v227, v227
	v_exp_f32_e32 v231, v214
	v_mfma_f32_16x16x32_f16 v[222:225], v[2:5], v[158:161], v[222:225]
	v_exp_f32_e32 v232, v215
	v_fma_f32 v226, -v226, v227, v227
	v_mfma_f32_16x16x32_f16 v[222:225], v[6:9], v[162:165], v[222:225]
	v_min_f32_e32 v233, s42, v216
	v_exp_f32_e32 v234, v217
	v_mfma_f32_16x16x32_f16 v[222:225], v[22:25], v[166:169], v[222:225]
	v_exp_f32_e32 v236, v218
	v_exp_f32_e32 v233, v233
	v_mfma_f32_16x16x32_f16 v[222:225], v[30:33], v[170:173], v[222:225]
	v_add_f32_e32 v232, 1.0, v232
	v_exp_f32_e32 v227, v219
	v_fma_f32 v235, v233, s41, s41
	v_rcp_f32_e32 v232, v232
	v_min_f32_e32 v228, s42, v220
	v_fma_f32 v235, v231, v235, v235
	v_rcp_f32_e32 v235, v235
	v_exp_f32_e32 v229, v221
	v_fma_f32 v231, -v233, v235, v235
	v_fma_f32 v201, v201, v232, v231
	v_exp_f32_e32 v228, v228
	v_min_f32_e32 v231, s42, v201
	v_exp_f32_e32 v231, v231
	v_add_f32_e32 v227, 1.0, v227
	v_add_f32_e32 v232, 1.0, v231
	v_mfma_f32_16x16x32_f16 v[146:149], v[130:133], v[158:161], v[146:149]
	v_fma_f32 v232, v234, v232, v232
	v_fma_f32 v230, v228, s41, s41
	v_rcp_f32_e32 v232, v232
	v_mfma_f32_16x16x32_f16 v[146:149], v[134:137], v[162:165], v[146:149]
	v_fma_f32 v231, -v231, v232, v232
	v_rcp_f32_e32 v227, v227
	v_cvt_pk_f16_f32 v246, v226, v231
	buffer_load_dwordx4 v[130:133], v189, s[72:75], s46 offen
	buffer_load_dwordx4 v[134:137], v208, s[72:75], s46 offen
	v_exp_f32_e32 v231, v222
	v_fma_f32 v230, v236, v230, v230
	v_exp_f32_e32 v232, v223
	s_waitcnt lgkmcnt(0)
	v_mfma_f32_16x16x32_f16 v[210:213], v[70:73], v[150:153], v[98:101]
	v_min_f32_e32 v233, s42, v224
	v_rcp_f32_e32 v230, v230
	v_exp_f32_e32 v234, v225
	v_mfma_f32_16x16x32_f16 v[214:217], v[74:77], v[150:153], v[102:105]
	v_exp_f32_e32 v233, v233
	v_fma_f32 v236, -v228, v230, v230
	v_add_f32_e32 v232, 1.0, v232
	v_fma_f32 v235, v233, s41, s41
	v_fma_f32 v198, v198, v227, v236
	v_rcp_f32_e32 v232, v232
	v_fma_f32 v235, v231, v235, v235
	v_min_f32_e32 v236, s42, v198
	v_rcp_f32_e32 v235, v235
	s_nop 0
	v_fma_f32 v231, -v233, v235, v235
	v_exp_f32_e32 v236, v236
	v_fma_f32 v199, v199, v232, v231
	v_min_f32_e32 v231, s42, v199
	v_add_f32_e32 v227, 1.0, v236
	v_exp_f32_e32 v231, v231
	v_fma_f32 v227, v229, v227, v227
	v_add_f32_e32 v232, 1.0, v231
	v_rcp_f32_e32 v227, v227
	v_fma_f32 v232, v234, v232, v232
	v_fma_f32 v236, -v236, v227, v227
	v_rcp_f32_e32 v232, v232
	s_nop 0
	v_fma_f32 v231, -v231, v232, v232
	v_cvt_pk_f16_f32 v247, v236, v231
	ds_write_b64 v250, v[246:247] offset:8192
	v_mfma_f32_16x16x32_f16 v[210:213], v[66:69], v[154:157], v[210:213]
	v_mfma_f32_16x16x32_f16 v[214:217], v[78:81], v[154:157], v[214:217]
	buffer_load_dwordx2 v[194:195], v209, s[52:55], s45 offen
	s_waitcnt lgkmcnt(0)
	s_barrier
	s_cmp_lt_u32 s46, 0xc0000
	s_cbranch_scc1 .Lmy_loopb
	s_nop 7
	ds_read_b128 v[158:161], v248 offset:0
	ds_read_b128 v[162:165], v248 offset:1024
	s_lshr_b32 s48, s35, 5
	v_and_b32_e32 v211, 15, v0
	v_bfe_u32 v212, v0, 4, 2
	v_and_b32_e32 v213, 31, v0
	v_bfe_u32 v214, v0, 5, 1
	v_add_u32_e32 v214, s48, v214
	s_lshl_b32 s49, s35, 4
	s_addk_i32 s49, 0x2000
	v_lshl_add_u32 v215, v212, 8, s49
	v_lshl_add_u32 v215, v211, 2, v215
	v_lshlrev_b32_e32 v216, 6, v213
	v_lshl_add_u32 v216, v214, 2, v216
	v_mul_u32_u24_e32 v217, 0x110, v214
	v_lshl_add_u32 v217, v213, 2, v217
	v_mul_u32_u24_e32 v218, 0x110, v211
	v_add_u32_e32 v219, 0x4000, v206
	v_add_u32_e32 v220, 0x14000, v206
	v_add_u32_e32 v221, 0x24000, v206
	v_add_u32_e32 v222, s34, v211
	v_lshlrev_b32_e32 v222, 9, v222
	v_add_u32_e32 v222, s35, v222
	v_lshl_add_u32 v222, v212, 4, v222
	s_waitcnt vmcnt(10) lgkmcnt(0)
	v_mfma_f32_16x16x32_f16 v[146:149], v[122:125], v[158:161], v[146:149]
	v_mfma_f32_16x16x32_f16 v[146:149], v[126:129], v[162:165], v[146:149]
	ds_read_b64 v[30:31], v219 offset:0
	ds_read_b64 v[32:33], v219 offset:4096
	ds_read_b64 v[34:35], v219 offset:8192
	ds_read_b64 v[36:37], v219 offset:12288
	ds_read_b64 v[38:39], v219 offset:16384
	ds_read_b64 v[40:41], v219 offset:20480
	ds_read_b64 v[42:43], v219 offset:24576
	ds_read_b64 v[44:45], v219 offset:28672
	s_waitcnt lgkmcnt(4)
	ds_read_b64 v[46:47], v219 offset:32768
	ds_read_b64 v[48:49], v219 offset:36864
	ds_read_b64 v[50:51], v219 offset:40960
	ds_read_b64 v[52:53], v219 offset:45056
	ds_read_b64 v[54:55], v219 offset:49152
	ds_read_b64 v[56:57], v219 offset:53248
	ds_read_b64 v[58:59], v219 offset:57344
	ds_read_b64 v[60:61], v219 offset:61440
	s_waitcnt lgkmcnt(4)
	ds_read_b64 v[62:63], v220 offset:0
	ds_read_b64 v[64:65], v220 offset:4096
	ds_read_b64 v[66:67], v220 offset:8192
	ds_read_b64 v[68:69], v220 offset:12288
	ds_read_b64 v[70:71], v220 offset:16384
	ds_read_b64 v[72:73], v220 offset:20480
	ds_read_b64 v[74:75], v220 offset:24576
	ds_read_b64 v[76:77], v220 offset:28672
	s_waitcnt lgkmcnt(4)
	ds_read_b64 v[78:79], v220 offset:32768
	ds_read_b64 v[80:81], v220 offset:36864
	ds_read_b64 v[82:83], v220 offset:40960
	ds_read_b64 v[84:85], v220 offset:45056
	ds_read_b64 v[86:87], v220 offset:49152
	ds_read_b64 v[88:89], v220 offset:53248
	ds_read_b64 v[90:91], v220 offset:57344
	ds_read_b64 v[92:93], v220 offset:61440
	s_waitcnt lgkmcnt(4)
	ds_read_b64 v[94:95], v221 offset:0
	ds_read_b64 v[96:97], v221 offset:4096
	ds_read_b64 v[98:99], v221 offset:8192
	ds_read_b64 v[100:101], v221 offset:12288
	ds_write2_b32 v215, v146, v147 offset1:16
	ds_write2_b32 v215, v148, v149 offset0:32 offset1:48
	s_waitcnt lgkmcnt(0)
	s_barrier
	ds_read2st64_b32 v[230:231], v216 offset0:32 offset1:48
	ds_read2st64_b32 v[232:233], v216 offset0:40 offset1:56
	v_cmp_gt_u32_e32 vcc, 18, v213
	s_waitcnt vmcnt(0) lgkmcnt(0)
	v_add_f32_e32 v223, v230, v231
	v_add_f32_e32 v224, v232, v233
	v_add_f32_e32 v223, v223, v254
	v_add_f32_e32 v224, v224, v255
	v_max_f32_e32 v223, 0, v223
	v_max_f32_e32 v224, 0, v224
	v_mov_b32_e32 v226, 0xf149f2ca
	v_cndmask_b32_e32 v224, v226, v224, vcc
	v_max_f32_e32 v225, v223, v224
	s_nop 1
	v_max_f32_dpp v226, v225, v225 quad_perm:[1,0,3,2] row_mask:0xf bank_mask:0xf
	s_nop 1
	v_max_f32_dpp v225, v226, v226 quad_perm:[2,3,0,1] row_mask:0xf bank_mask:0xf
	s_nop 1
	v_max_f32_dpp v226, v225, v225 row_half_mirror row_mask:0xf bank_mask:0xf
	s_nop 1
	v_max_f32_dpp v225, v226, v226 row_mirror row_mask:0xf bank_mask:0xf
	ds_swizzle_b32 v226, v225 offset:swizzle(SWAP,16)
	s_waitcnt lgkmcnt(0)
	v_max_f32_e32 v225, v225, v226
	v_sub_f32_e32 v223, v223, v225
	v_sub_f32_e32 v224, v224, v225
	v_mul_f32_e32 v223, 0x3fb8aa3b, v223
	v_mul_f32_e32 v224, 0x3fb8aa3b, v224
	v_exp_f32_e32 v227, v223
	v_exp_f32_e32 v228, v224
	s_nop 0
	v_add_f32_e32 v229, v227, v228
	s_nop 1
	v_add_f32_dpp v226, v229, v229 quad_perm:[1,0,3,2] row_mask:0xf bank_mask:0xf
	s_nop 1
	v_add_f32_dpp v229, v226, v226 quad_perm:[2,3,0,1] row_mask:0xf bank_mask:0xf
	s_nop 1
	v_add_f32_dpp v226, v229, v229 row_half_mirror row_mask:0xf bank_mask:0xf
	s_nop 1
	v_add_f32_dpp v229, v226, v226 row_mirror row_mask:0xf bank_mask:0xf
	ds_swizzle_b32 v226, v229 offset:swizzle(SWAP,16)
	s_waitcnt lgkmcnt(0)
	v_add_f32_e32 v229, v229, v226
	v_rcp_f32_e32 v234, v229
	s_nop 0
	v_mul_f32_e32 v227, v227, v234
	v_mul_f32_e32 v228, v228, v234
	ds_write_b32 v217, v227
	ds_write_b32 v217, v228 offset:128
	s_waitcnt lgkmcnt(0)
	s_barrier
	ds_read_b128 v[102:105], v218 offset:0
	ds_read_b128 v[106:109], v218 offset:16
	ds_read_b128 v[110:113], v218 offset:32
	ds_read_b128 v[114:117], v218 offset:48
	ds_read_b128 v[118:121], v218 offset:64
	ds_read_b128 v[122:125], v218 offset:80
	ds_read_b128 v[126:129], v218 offset:96
	ds_read_b128 v[130:133], v218 offset:112
	ds_read_b128 v[134:137], v218 offset:128
	ds_read_b128 v[138:141], v218 offset:144
	ds_read_b128 v[142:145], v218 offset:160
	ds_read_b128 v[146:149], v218 offset:176
	ds_read_b128 v[150:153], v218 offset:192
	v_mov_b32_e32 v154, 0
	v_mov_b32_e32 v155, 0
	v_mov_b32_e32 v156, 0
	v_mov_b32_e32 v157, 0
	s_waitcnt vmcnt(0) lgkmcnt(0)
	v_fma_mix_f32 v154, v174, v102, v154 op_sel_hi:[1,0,0]
	v_fma_mix_f32 v155, v174, v102, v155 op_sel:[1,0,0] op_sel_hi:[1,0,0]
	v_fma_mix_f32 v156, v175, v102, v156 op_sel_hi:[1,0,0]
	v_fma_mix_f32 v157, v175, v102, v157 op_sel:[1,0,0] op_sel_hi:[1,0,0]
	v_fma_mix_f32 v154, v176, v103, v154 op_sel_hi:[1,0,0]
	v_fma_mix_f32 v155, v176, v103, v155 op_sel:[1,0,0] op_sel_hi:[1,0,0]
	v_fma_mix_f32 v156, v177, v103, v156 op_sel_hi:[1,0,0]
	v_fma_mix_f32 v157, v177, v103, v157 op_sel:[1,0,0] op_sel_hi:[1,0,0]
	v_fma_mix_f32 v154, v178, v104, v154 op_sel_hi:[1,0,0]
	v_fma_mix_f32 v155, v178, v104, v155 op_sel:[1,0,0] op_sel_hi:[1,0,0]
	v_fma_mix_f32 v156, v179, v104, v156 op_sel_hi:[1,0,0]
	v_fma_mix_f32 v157, v179, v104, v157 op_sel:[1,0,0] op_sel_hi:[1,0,0]
	v_fma_mix_f32 v154, v180, v105, v154 op_sel_hi:[1,0,0]
	v_fma_mix_f32 v155, v180, v105, v155 op_sel:[1,0,0] op_sel_hi:[1,0,0]
	v_fma_mix_f32 v156, v181, v105, v156 op_sel_hi:[1,0,0]
	v_fma_mix_f32 v157, v181, v105, v157 op_sel:[1,0,0] op_sel_hi:[1,0,0]
	v_fma_mix_f32 v154, v182, v106, v154 op_sel_hi:[1,0,0]
	v_fma_mix_f32 v155, v182, v106, v155 op_sel:[1,0,0] op_sel_hi:[1,0,0]
	v_fma_mix_f32 v156, v183, v106, v156 op_sel_hi:[1,0,0]
	v_fma_mix_f32 v157, v183, v106, v157 op_sel:[1,0,0] op_sel_hi:[1,0,0]
	v_fma_mix_f32 v154, v184, v107, v154 op_sel_hi:[1,0,0]
	v_fma_mix_f32 v155, v184, v107, v155 op_sel:[1,0,0] op_sel_hi:[1,0,0]
	v_fma_mix_f32 v156, v185, v107, v156 op_sel_hi:[1,0,0]
	v_fma_mix_f32 v157, v185, v107, v157 op_sel:[1,0,0] op_sel_hi:[1,0,0]
	v_fma_mix_f32 v154, v237, v108, v154 op_sel_hi:[1,0,0]
	v_fma_mix_f32 v155, v237, v108, v155 op_sel:[1,0,0] op_sel_hi:[1,0,0]
	v_fma_mix_f32 v156, v238, v108, v156 op_sel_hi:[1,0,0]
	v_fma_mix_f32 v157, v238, v108, v157 op_sel:[1,0,0] op_sel_hi:[1,0,0]
	v_fma_mix_f32 v154, v239, v109, v154 op_sel_hi:[1,0,0]
	v_fma_mix_f32 v155, v239, v109, v155 op_sel:[1,0,0] op_sel_hi:[1,0,0]
	v_fma_mix_f32 v156, v240, v109, v156 op_sel_hi:[1,0,0]
	v_fma_mix_f32 v157, v240, v109, v157 op_sel:[1,0,0] op_sel_hi:[1,0,0]
	v_fma_mix_f32 v154, v241, v110, v154 op_sel_hi:[1,0,0]
	v_fma_mix_f32 v155, v241, v110, v155 op_sel:[1,0,0] op_sel_hi:[1,0,0]
	v_fma_mix_f32 v156, v242, v110, v156 op_sel_hi:[1,0,0]
	v_fma_mix_f32 v157, v242, v110, v157 op_sel:[1,0,0] op_sel_hi:[1,0,0]
	v_fma_mix_f32 v154, v243, v111, v154 op_sel_hi:[1,0,0]
	v_fma_mix_f32 v155, v243, v111, v155 op_sel:[1,0,0] op_sel_hi:[1,0,0]
	v_fma_mix_f32 v156, v244, v111, v156 op_sel_hi:[1,0,0]
	v_fma_mix_f32 v157, v244, v111, v157 op_sel:[1,0,0] op_sel_hi:[1,0,0]
	v_fma_mix_f32 v154, v245, v112, v154 op_sel_hi:[1,0,0]
	v_fma_mix_f32 v155, v245, v112, v155 op_sel:[1,0,0] op_sel_hi:[1,0,0]
	v_fma_mix_f32 v156, v187, v112, v156 op_sel_hi:[1,0,0]
	v_fma_mix_f32 v157, v187, v112, v157 op_sel:[1,0,0] op_sel_hi:[1,0,0]
	v_fma_mix_f32 v154, v188, v113, v154 op_sel_hi:[1,0,0]
	v_fma_mix_f32 v155, v188, v113, v155 op_sel:[1,0,0] op_sel_hi:[1,0,0]
	v_fma_mix_f32 v156, v202, v113, v156 op_sel_hi:[1,0,0]
	v_fma_mix_f32 v157, v202, v113, v157 op_sel:[1,0,0] op_sel_hi:[1,0,0]
	v_fma_mix_f32 v154, v203, v114, v154 op_sel_hi:[1,0,0]
	v_fma_mix_f32 v155, v203, v114, v155 op_sel:[1,0,0] op_sel_hi:[1,0,0]
	v_fma_mix_f32 v156, v204, v114, v156 op_sel_hi:[1,0,0]
	v_fma_mix_f32 v157, v204, v114, v157 op_sel:[1,0,0] op_sel_hi:[1,0,0]
	v_fma_mix_f32 v154, v205, v115, v154 op_sel_hi:[1,0,0]
	v_fma_mix_f32 v155, v205, v115, v155 op_sel:[1,0,0] op_sel_hi:[1,0,0]
	v_fma_mix_f32 v156, v207, v115, v156 op_sel_hi:[1,0,0]
	v_fma_mix_f32 v157, v207, v115, v157 op_sel:[1,0,0] op_sel_hi:[1,0,0]
	v_fma_mix_f32 v154, v30, v116, v154 op_sel_hi:[1,0,0]
	v_fma_mix_f32 v155, v30, v116, v155 op_sel:[1,0,0] op_sel_hi:[1,0,0]
	v_fma_mix_f32 v156, v31, v116, v156 op_sel_hi:[1,0,0]
	v_fma_mix_f32 v157, v31, v116, v157 op_sel:[1,0,0] op_sel_hi:[1,0,0]
	v_fma_mix_f32 v154, v32, v117, v154 op_sel_hi:[1,0,0]
	v_fma_mix_f32 v155, v32, v117, v155 op_sel:[1,0,0] op_sel_hi:[1,0,0]
	v_fma_mix_f32 v156, v33, v117, v156 op_sel_hi:[1,0,0]
	v_fma_mix_f32 v157, v33, v117, v157 op_sel:[1,0,0] op_sel_hi:[1,0,0]
	v_fma_mix_f32 v154, v34, v118, v154 op_sel_hi:[1,0,0]
	v_fma_mix_f32 v155, v34, v118, v155 op_sel:[1,0,0] op_sel_hi:[1,0,0]
	v_fma_mix_f32 v156, v35, v118, v156 op_sel_hi:[1,0,0]
	v_fma_mix_f32 v157, v35, v118, v157 op_sel:[1,0,0] op_sel_hi:[1,0,0]
	v_fma_mix_f32 v154, v36, v119, v154 op_sel_hi:[1,0,0]
	v_fma_mix_f32 v155, v36, v119, v155 op_sel:[1,0,0] op_sel_hi:[1,0,0]
	v_fma_mix_f32 v156, v37, v119, v156 op_sel_hi:[1,0,0]
	v_fma_mix_f32 v157, v37, v119, v157 op_sel:[1,0,0] op_sel_hi:[1,0,0]
	v_fma_mix_f32 v154, v38, v120, v154 op_sel_hi:[1,0,0]
	v_fma_mix_f32 v155, v38, v120, v155 op_sel:[1,0,0] op_sel_hi:[1,0,0]
	v_fma_mix_f32 v156, v39, v120, v156 op_sel_hi:[1,0,0]
	v_fma_mix_f32 v157, v39, v120, v157 op_sel:[1,0,0] op_sel_hi:[1,0,0]
	v_fma_mix_f32 v154, v40, v121, v154 op_sel_hi:[1,0,0]
	v_fma_mix_f32 v155, v40, v121, v155 op_sel:[1,0,0] op_sel_hi:[1,0,0]
	v_fma_mix_f32 v156, v41, v121, v156 op_sel_hi:[1,0,0]
	v_fma_mix_f32 v157, v41, v121, v157 op_sel:[1,0,0] op_sel_hi:[1,0,0]
	v_fma_mix_f32 v154, v42, v122, v154 op_sel_hi:[1,0,0]
	v_fma_mix_f32 v155, v42, v122, v155 op_sel:[1,0,0] op_sel_hi:[1,0,0]
	v_fma_mix_f32 v156, v43, v122, v156 op_sel_hi:[1,0,0]
	v_fma_mix_f32 v157, v43, v122, v157 op_sel:[1,0,0] op_sel_hi:[1,0,0]
	v_fma_mix_f32 v154, v44, v123, v154 op_sel_hi:[1,0,0]
	v_fma_mix_f32 v155, v44, v123, v155 op_sel:[1,0,0] op_sel_hi:[1,0,0]
	v_fma_mix_f32 v156, v45, v123, v156 op_sel_hi:[1,0,0]
	v_fma_mix_f32 v157, v45, v123, v157 op_sel:[1,0,0] op_sel_hi:[1,0,0]
	v_fma_mix_f32 v154, v46, v124, v154 op_sel_hi:[1,0,0]
	v_fma_mix_f32 v155, v46, v124, v155 op_sel:[1,0,0] op_sel_hi:[1,0,0]
	v_fma_mix_f32 v156, v47, v124, v156 op_sel_hi:[1,0,0]
	v_fma_mix_f32 v157, v47, v124, v157 op_sel:[1,0,0] op_sel_hi:[1,0,0]
	v_fma_mix_f32 v154, v48, v125, v154 op_sel_hi:[1,0,0]
	v_fma_mix_f32 v155, v48, v125, v155 op_sel:[1,0,0] op_sel_hi:[1,0,0]
	v_fma_mix_f32 v156, v49, v125, v156 op_sel_hi:[1,0,0]
	v_fma_mix_f32 v157, v49, v125, v157 op_sel:[1,0,0] op_sel_hi:[1,0,0]
	v_fma_mix_f32 v154, v50, v126, v154 op_sel_hi:[1,0,0]
	v_fma_mix_f32 v155, v50, v126, v155 op_sel:[1,0,0] op_sel_hi:[1,0,0]
	v_fma_mix_f32 v156, v51, v126, v156 op_sel_hi:[1,0,0]
	v_fma_mix_f32 v157, v51, v126, v157 op_sel:[1,0,0] op_sel_hi:[1,0,0]
	v_fma_mix_f32 v154, v52, v127, v154 op_sel_hi:[1,0,0]
	v_fma_mix_f32 v155, v52, v127, v155 op_sel:[1,0,0] op_sel_hi:[1,0,0]
	v_fma_mix_f32 v156, v53, v127, v156 op_sel_hi:[1,0,0]
	v_fma_mix_f32 v157, v53, v127, v157 op_sel:[1,0,0] op_sel_hi:[1,0,0]
	v_fma_mix_f32 v154, v54, v128, v154 op_sel_hi:[1,0,0]
	v_fma_mix_f32 v155, v54, v128, v155 op_sel:[1,0,0] op_sel_hi:[1,0,0]
	v_fma_mix_f32 v156, v55, v128, v156 op_sel_hi:[1,0,0]
	v_fma_mix_f32 v157, v55, v128, v157 op_sel:[1,0,0] op_sel_hi:[1,0,0]
	v_fma_mix_f32 v154, v56, v129, v154 op_sel_hi:[1,0,0]
	v_fma_mix_f32 v155, v56, v129, v155 op_sel:[1,0,0] op_sel_hi:[1,0,0]
	v_fma_mix_f32 v156, v57, v129, v156 op_sel_hi:[1,0,0]
	v_fma_mix_f32 v157, v57, v129, v157 op_sel:[1,0,0] op_sel_hi:[1,0,0]
	v_fma_mix_f32 v154, v58, v130, v154 op_sel_hi:[1,0,0]
	v_fma_mix_f32 v155, v58, v130, v155 op_sel:[1,0,0] op_sel_hi:[1,0,0]
	v_fma_mix_f32 v156, v59, v130, v156 op_sel_hi:[1,0,0]
	v_fma_mix_f32 v157, v59, v130, v157 op_sel:[1,0,0] op_sel_hi:[1,0,0]
	v_fma_mix_f32 v154, v60, v131, v154 op_sel_hi:[1,0,0]
	v_fma_mix_f32 v155, v60, v131, v155 op_sel:[1,0,0] op_sel_hi:[1,0,0]
	v_fma_mix_f32 v156, v61, v131, v156 op_sel_hi:[1,0,0]
	v_fma_mix_f32 v157, v61, v131, v157 op_sel:[1,0,0] op_sel_hi:[1,0,0]
	v_fma_mix_f32 v154, v62, v132, v154 op_sel_hi:[1,0,0]
	v_fma_mix_f32 v155, v62, v132, v155 op_sel:[1,0,0] op_sel_hi:[1,0,0]
	v_fma_mix_f32 v156, v63, v132, v156 op_sel_hi:[1,0,0]
	v_fma_mix_f32 v157, v63, v132, v157 op_sel:[1,0,0] op_sel_hi:[1,0,0]
	v_fma_mix_f32 v154, v64, v133, v154 op_sel_hi:[1,0,0]
	v_fma_mix_f32 v155, v64, v133, v155 op_sel:[1,0,0] op_sel_hi:[1,0,0]
	v_fma_mix_f32 v156, v65, v133, v156 op_sel_hi:[1,0,0]
	v_fma_mix_f32 v157, v65, v133, v157 op_sel:[1,0,0] op_sel_hi:[1,0,0]
	v_fma_mix_f32 v154, v66, v134, v154 op_sel_hi:[1,0,0]
	v_fma_mix_f32 v155, v66, v134, v155 op_sel:[1,0,0] op_sel_hi:[1,0,0]
	v_fma_mix_f32 v156, v67, v134, v156 op_sel_hi:[1,0,0]
	v_fma_mix_f32 v157, v67, v134, v157 op_sel:[1,0,0] op_sel_hi:[1,0,0]
	v_fma_mix_f32 v154, v68, v135, v154 op_sel_hi:[1,0,0]
	v_fma_mix_f32 v155, v68, v135, v155 op_sel:[1,0,0] op_sel_hi:[1,0,0]
	v_fma_mix_f32 v156, v69, v135, v156 op_sel_hi:[1,0,0]
	v_fma_mix_f32 v157, v69, v135, v157 op_sel:[1,0,0] op_sel_hi:[1,0,0]
	v_fma_mix_f32 v154, v70, v136, v154 op_sel_hi:[1,0,0]
	v_fma_mix_f32 v155, v70, v136, v155 op_sel:[1,0,0] op_sel_hi:[1,0,0]
	v_fma_mix_f32 v156, v71, v136, v156 op_sel_hi:[1,0,0]
	v_fma_mix_f32 v157, v71, v136, v157 op_sel:[1,0,0] op_sel_hi:[1,0,0]
	v_fma_mix_f32 v154, v72, v137, v154 op_sel_hi:[1,0,0]
	v_fma_mix_f32 v155, v72, v137, v155 op_sel:[1,0,0] op_sel_hi:[1,0,0]
	v_fma_mix_f32 v156, v73, v137, v156 op_sel_hi:[1,0,0]
	v_fma_mix_f32 v157, v73, v137, v157 op_sel:[1,0,0] op_sel_hi:[1,0,0]
	v_fma_mix_f32 v154, v74, v138, v154 op_sel_hi:[1,0,0]
	v_fma_mix_f32 v155, v74, v138, v155 op_sel:[1,0,0] op_sel_hi:[1,0,0]
	v_fma_mix_f32 v156, v75, v138, v156 op_sel_hi:[1,0,0]
	v_fma_mix_f32 v157, v75, v138, v157 op_sel:[1,0,0] op_sel_hi:[1,0,0]
	v_fma_mix_f32 v154, v76, v139, v154 op_sel_hi:[1,0,0]
	v_fma_mix_f32 v155, v76, v139, v155 op_sel:[1,0,0] op_sel_hi:[1,0,0]
	v_fma_mix_f32 v156, v77, v139, v156 op_sel_hi:[1,0,0]
	v_fma_mix_f32 v157, v77, v139, v157 op_sel:[1,0,0] op_sel_hi:[1,0,0]
	v_fma_mix_f32 v154, v78, v140, v154 op_sel_hi:[1,0,0]
	v_fma_mix_f32 v155, v78, v140, v155 op_sel:[1,0,0] op_sel_hi:[1,0,0]
	v_fma_mix_f32 v156, v79, v140, v156 op_sel_hi:[1,0,0]
	v_fma_mix_f32 v157, v79, v140, v157 op_sel:[1,0,0] op_sel_hi:[1,0,0]
	v_fma_mix_f32 v154, v80, v141, v154 op_sel_hi:[1,0,0]
	v_fma_mix_f32 v155, v80, v141, v155 op_sel:[1,0,0] op_sel_hi:[1,0,0]
	v_fma_mix_f32 v156, v81, v141, v156 op_sel_hi:[1,0,0]
	v_fma_mix_f32 v157, v81, v141, v157 op_sel:[1,0,0] op_sel_hi:[1,0,0]
	v_fma_mix_f32 v154, v82, v142, v154 op_sel_hi:[1,0,0]
	v_fma_mix_f32 v155, v82, v142, v155 op_sel:[1,0,0] op_sel_hi:[1,0,0]
	v_fma_mix_f32 v156, v83, v142, v156 op_sel_hi:[1,0,0]
	v_fma_mix_f32 v157, v83, v142, v157 op_sel:[1,0,0] op_sel_hi:[1,0,0]
	v_fma_mix_f32 v154, v84, v143, v154 op_sel_hi:[1,0,0]
	v_fma_mix_f32 v155, v84, v143, v155 op_sel:[1,0,0] op_sel_hi:[1,0,0]
	v_fma_mix_f32 v156, v85, v143, v156 op_sel_hi:[1,0,0]
	v_fma_mix_f32 v157, v85, v143, v157 op_sel:[1,0,0] op_sel_hi:[1,0,0]
	v_fma_mix_f32 v154, v86, v144, v154 op_sel_hi:[1,0,0]
	v_fma_mix_f32 v155, v86, v144, v155 op_sel:[1,0,0] op_sel_hi:[1,0,0]
	v_fma_mix_f32 v156, v87, v144, v156 op_sel_hi:[1,0,0]
	v_fma_mix_f32 v157, v87, v144, v157 op_sel:[1,0,0] op_sel_hi:[1,0,0]
	v_fma_mix_f32 v154, v88, v145, v154 op_sel_hi:[1,0,0]
	v_fma_mix_f32 v155, v88, v145, v155 op_sel:[1,0,0] op_sel_hi:[1,0,0]
	v_fma_mix_f32 v156, v89, v145, v156 op_sel_hi:[1,0,0]
	v_fma_mix_f32 v157, v89, v145, v157 op_sel:[1,0,0] op_sel_hi:[1,0,0]
	v_fma_mix_f32 v154, v90, v146, v154 op_sel_hi:[1,0,0]
	v_fma_mix_f32 v155, v90, v146, v155 op_sel:[1,0,0] op_sel_hi:[1,0,0]
	v_fma_mix_f32 v156, v91, v146, v156 op_sel_hi:[1,0,0]
	v_fma_mix_f32 v157, v91, v146, v157 op_sel:[1,0,0] op_sel_hi:[1,0,0]
	v_fma_mix_f32 v154, v92, v147, v154 op_sel_hi:[1,0,0]
	v_fma_mix_f32 v155, v92, v147, v155 op_sel:[1,0,0] op_sel_hi:[1,0,0]
	v_fma_mix_f32 v156, v93, v147, v156 op_sel_hi:[1,0,0]
	v_fma_mix_f32 v157, v93, v147, v157 op_sel:[1,0,0] op_sel_hi:[1,0,0]
	v_fma_mix_f32 v154, v94, v148, v154 op_sel_hi:[1,0,0]
	v_fma_mix_f32 v155, v94, v148, v155 op_sel:[1,0,0] op_sel_hi:[1,0,0]
	v_fma_mix_f32 v156, v95, v148, v156 op_sel_hi:[1,0,0]
	v_fma_mix_f32 v157, v95, v148, v157 op_sel:[1,0,0] op_sel_hi:[1,0,0]
	v_fma_mix_f32 v154, v96, v149, v154 op_sel_hi:[1,0,0]
	v_fma_mix_f32 v155, v96, v149, v155 op_sel:[1,0,0] op_sel_hi:[1,0,0]
	v_fma_mix_f32 v156, v97, v149, v156 op_sel_hi:[1,0,0]
	v_fma_mix_f32 v157, v97, v149, v157 op_sel:[1,0,0] op_sel_hi:[1,0,0]
	v_fma_mix_f32 v154, v98, v150, v154 op_sel_hi:[1,0,0]
	v_fma_mix_f32 v155, v98, v150, v155 op_sel:[1,0,0] op_sel_hi:[1,0,0]
	v_fma_mix_f32 v156, v99, v150, v156 op_sel_hi:[1,0,0]
	v_fma_mix_f32 v157, v99, v150, v157 op_sel:[1,0,0] op_sel_hi:[1,0,0]
	v_fma_mix_f32 v154, v100, v151, v154 op_sel_hi:[1,0,0]
	v_fma_mix_f32 v155, v100, v151, v155 op_sel:[1,0,0] op_sel_hi:[1,0,0]
	v_fma_mix_f32 v156, v101, v151, v156 op_sel_hi:[1,0,0]
	v_fma_mix_f32 v157, v101, v151, v157 op_sel:[1,0,0] op_sel_hi:[1,0,0]
	global_store_dwordx4 v222, v[154:157], s[8:9]
	s_endpgm
